# GEMM K-loops: LDS-DMA issue pairs moved from the inter-barrier gap to behind the first two MFMAs of the phase (phases without vmcnt wait)
# baseline (speedup 1.0000x reference)
.LBB0_191:
	s_ashr_i32 s61, s60, 31
	s_lshl_b64 s[62:63], s[60:61], 19
	s_add_u32 s62, s12, s62
	s_addc_u32 s63, s13, s63
	s_ashr_i32 s59, s58, 31
	s_lshl_b64 s[64:65], s[58:59], 19
	s_add_u32 s64, s14, s64
	s_addc_u32 s65, s15, s65
	s_andn2_b64 vcc, exec, s[30:31]
	s_cbranch_vccnz .LBB0_195
	v_cmp_lt_i64_e32 vcc, s[68:69], v[142:143]
	s_and_b64 s[68:69], vcc, exec
	s_cselect_b32 s9, s63, s11
	s_cselect_b32 s59, s62, s10
	s_cselect_b32 s61, s65, s67
	s_cselect_b32 s86, s64, s66
	s_add_u32 s10, s10, 0x40080
	s_addc_u32 s11, s11, 0
	s_add_u32 s87, s66, 0x100
	s_addc_u32 s88, s67, 0
	s_mov_b32 s66, 0
	s_waitcnt vmcnt(0)
	v_add_u32_e32 v154, s77, v157
	ds_read_b128 v[146:149], v154
	ds_read_b128 v[150:153], v154 offset:1024
	ds_read_b128 v[164:167], v154 offset:2048
	ds_read_b128 v[168:171], v154 offset:3072
	s_add_i32 s89, s66, 2
	s_add_u32 s67, s10, 0xfffc0080
	s_addc_u32 s68, s11, -1
	s_cmp_eq_u32 s75, s66
	s_cselect_b32 s66, s86, s87
	s_cselect_b32 s69, s9, s68
	s_cselect_b32 s68, s59, s67
	s_cselect_b32 s67, s61, s88
	v_lshl_add_u64 v[206:207], s[10:11], 0, v[138:139]
	s_add_i32 m0, s52, 0xc000
	ds_read_b128 v[172:175], v159
	ds_read_b128 v[176:179], v159 offset:1024
	ds_read_b128 v[180:183], v159 offset:2048
	ds_read_b128 v[184:187], v159 offset:3072
	ds_read_b128 v[188:191], v159 offset:4096
	ds_read_b128 v[192:195], v159 offset:5120
	ds_read_b128 v[198:201], v159 offset:6144
	ds_read_b128 v[202:205], v159 offset:7168
	global_load_lds_dwordx4 v[206:207], off
	v_lshl_add_u64 v[206:207], s[10:11], 0, v[140:141]
	s_add_i32 m0, s52, 0xe000
	s_nop 0
	global_load_lds_dwordx4 v[206:207], off
	s_waitcnt lgkmcnt(8)
	s_barrier
	s_setprio 1
	s_waitcnt lgkmcnt(0)
	v_mfma_i32_16x16x64_i8 v[62:65], v[146:149], v[172:175], 0
	v_mfma_i32_16x16x64_i8 v[58:61], v[164:167], v[172:175], 0
	v_mfma_i32_16x16x64_i8 v[54:57], v[146:149], v[180:183], 0
	v_mfma_i32_16x16x64_i8 v[50:53], v[164:167], v[180:183], 0
	v_mfma_i32_16x16x64_i8 v[46:49], v[146:149], v[188:191], 0
	v_mfma_i32_16x16x64_i8 v[42:45], v[164:167], v[188:191], 0
	v_mfma_i32_16x16x64_i8 v[38:41], v[146:149], v[198:201], 0
	v_mfma_i32_16x16x64_i8 v[34:37], v[164:167], v[198:201], 0
	v_mfma_i32_16x16x64_i8 v[62:65], v[150:153], v[176:179], v[62:65]
	v_mfma_i32_16x16x64_i8 v[58:61], v[168:171], v[176:179], v[58:61]
	v_mfma_i32_16x16x64_i8 v[54:57], v[150:153], v[184:187], v[54:57]
	v_mfma_i32_16x16x64_i8 v[50:53], v[168:171], v[184:187], v[50:53]
	v_mfma_i32_16x16x64_i8 v[46:49], v[150:153], v[192:195], v[46:49]
	v_mfma_i32_16x16x64_i8 v[42:45], v[168:171], v[192:195], v[42:45]
	v_mfma_i32_16x16x64_i8 v[38:41], v[150:153], v[202:205], v[38:41]
	v_mfma_i32_16x16x64_i8 v[34:37], v[168:171], v[202:205], v[34:37]
	s_setprio 0
	s_barrier
	s_add_i32 s90, s77, s4
	v_add_u32_e32 v154, s78, v157
	ds_read_b128 v[206:209], v154
	ds_read_b128 v[210:213], v154 offset:1024
	ds_read_b128 v[214:217], v154 offset:2048
	ds_read_b128 v[218:221], v154 offset:3072
	s_barrier
	s_setprio 1
	s_waitcnt lgkmcnt(0)
	v_mfma_i32_16x16x64_i8 v[126:129], v[206:209], v[172:175], 0
	v_lshl_add_u64 v[222:223], s[66:67], 0, v[134:135]
	s_mov_b32 m0, s90
	s_nop 0
	global_load_lds_dwordx4 v[222:223], off
	v_mfma_i32_16x16x64_i8 v[122:125], v[214:217], v[172:175], 0
	v_lshl_add_u64 v[224:225], s[66:67], 0, v[130:131]
	s_add_i32 m0, s90, 0x2000
	s_nop 0
	global_load_lds_dwordx4 v[224:225], off
	ds_read_b128 v[172:175], v159 offset:16384
	v_mfma_i32_16x16x64_i8 v[118:121], v[206:209], v[180:183], 0
	v_mfma_i32_16x16x64_i8 v[114:117], v[214:217], v[180:183], 0
	ds_read_b128 v[180:183], v159 offset:18432
	v_mfma_i32_16x16x64_i8 v[110:113], v[206:209], v[188:191], 0
	v_mfma_i32_16x16x64_i8 v[106:109], v[214:217], v[188:191], 0
	ds_read_b128 v[188:191], v159 offset:20480
	v_mfma_i32_16x16x64_i8 v[102:105], v[206:209], v[198:201], 0
	v_mfma_i32_16x16x64_i8 v[98:101], v[214:217], v[198:201], 0
	ds_read_b128 v[198:201], v159 offset:22528
	v_mfma_i32_16x16x64_i8 v[126:129], v[210:213], v[176:179], v[126:129]
	v_mfma_i32_16x16x64_i8 v[122:125], v[218:221], v[176:179], v[122:125]
	ds_read_b128 v[176:179], v159 offset:17408
	v_mfma_i32_16x16x64_i8 v[118:121], v[210:213], v[184:187], v[118:121]
	v_mfma_i32_16x16x64_i8 v[114:117], v[218:221], v[184:187], v[114:117]
	ds_read_b128 v[184:187], v159 offset:19456
	v_mfma_i32_16x16x64_i8 v[110:113], v[210:213], v[192:195], v[110:113]
	v_mfma_i32_16x16x64_i8 v[106:109], v[218:221], v[192:195], v[106:109]
	ds_read_b128 v[192:195], v159 offset:21504
	v_mfma_i32_16x16x64_i8 v[102:105], v[210:213], v[202:205], v[102:105]
	v_mfma_i32_16x16x64_i8 v[98:101], v[218:221], v[202:205], v[98:101]
	ds_read_b128 v[202:205], v159 offset:23552
	s_setprio 0
	s_barrier
	s_barrier
	s_setprio 1
	s_waitcnt lgkmcnt(0)
	v_mfma_i32_16x16x64_i8 v[30:33], v[146:149], v[172:175], 0
	s_mov_b32 m0, s52
	v_lshl_add_u64 v[226:227], s[68:69], 0, v[136:137]
	s_nop 0
	global_load_lds_dwordx4 v[226:227], off
	v_mfma_i32_16x16x64_i8 v[26:29], v[164:167], v[172:175], 0
	v_lshl_add_u64 v[228:229], s[68:69], 0, v[132:133]
	s_mov_b32 m0, s53
	s_nop 0
	global_load_lds_dwordx4 v[228:229], off
	v_mfma_i32_16x16x64_i8 v[22:25], v[146:149], v[180:183], 0
	v_mfma_i32_16x16x64_i8 v[18:21], v[164:167], v[180:183], 0
	v_mfma_i32_16x16x64_i8 v[14:17], v[146:149], v[188:191], 0
	v_mfma_i32_16x16x64_i8 v[10:13], v[164:167], v[188:191], 0
	v_mfma_i32_16x16x64_i8 v[6:9], v[146:149], v[198:201], 0
	v_mfma_i32_16x16x64_i8 v[2:5], v[164:167], v[198:201], 0
	v_mfma_i32_16x16x64_i8 v[30:33], v[150:153], v[176:179], v[30:33]
	v_mfma_i32_16x16x64_i8 v[26:29], v[168:171], v[176:179], v[26:29]
	v_mfma_i32_16x16x64_i8 v[22:25], v[150:153], v[184:187], v[22:25]
	v_mfma_i32_16x16x64_i8 v[18:21], v[168:171], v[184:187], v[18:21]
	v_mfma_i32_16x16x64_i8 v[14:17], v[150:153], v[192:195], v[14:17]
	v_mfma_i32_16x16x64_i8 v[10:13], v[168:171], v[192:195], v[10:13]
	v_mfma_i32_16x16x64_i8 v[6:9], v[150:153], v[202:205], v[6:9]
	v_mfma_i32_16x16x64_i8 v[2:5], v[168:171], v[202:205], v[2:5]
	s_setprio 0
	s_barrier
	s_add_u32 s90, s66, 0x40000
	s_addc_u32 s91, s67, 0
	s_add_i32 s92, s78, s4
	v_lshl_add_u64 v[146:147], s[90:91], 0, v[134:135]
	s_mov_b32 m0, s92
	s_nop 0
	global_load_lds_dwordx4 v[146:147], off
	v_lshl_add_u64 v[146:147], s[90:91], 0, v[130:131]
	s_add_i32 m0, s92, 0x2000
	s_nop 0
	global_load_lds_dwordx4 v[146:147], off
	s_waitcnt vmcnt(6)
	s_barrier
	s_setprio 1
	v_mfma_i32_16x16x64_i8 v[94:97], v[206:209], v[172:175], 0
	v_mfma_i32_16x16x64_i8 v[90:93], v[214:217], v[172:175], 0
	ds_read_b128 v[172:175], v159 offset:32768
	v_mfma_i32_16x16x64_i8 v[86:89], v[206:209], v[180:183], 0
	v_mfma_i32_16x16x64_i8 v[82:85], v[214:217], v[180:183], 0
	ds_read_b128 v[180:183], v159 offset:34816
	v_mfma_i32_16x16x64_i8 v[78:81], v[206:209], v[188:191], 0
	v_mfma_i32_16x16x64_i8 v[74:77], v[214:217], v[188:191], 0
	ds_read_b128 v[188:191], v159 offset:36864
	v_mfma_i32_16x16x64_i8 v[70:73], v[206:209], v[198:201], 0
	v_mfma_i32_16x16x64_i8 v[66:69], v[214:217], v[198:201], 0
	ds_read_b128 v[198:201], v159 offset:38912
	v_mfma_i32_16x16x64_i8 v[94:97], v[210:213], v[176:179], v[94:97]
	v_mfma_i32_16x16x64_i8 v[90:93], v[218:221], v[176:179], v[90:93]
	ds_read_b128 v[176:179], v159 offset:33792
	v_mfma_i32_16x16x64_i8 v[86:89], v[210:213], v[184:187], v[86:89]
	v_mfma_i32_16x16x64_i8 v[82:85], v[218:221], v[184:187], v[82:85]
	ds_read_b128 v[184:187], v159 offset:35840
	v_mfma_i32_16x16x64_i8 v[78:81], v[210:213], v[192:195], v[78:81]
	v_mfma_i32_16x16x64_i8 v[74:77], v[218:221], v[192:195], v[74:77]
	ds_read_b128 v[192:195], v159 offset:37888
	v_mfma_i32_16x16x64_i8 v[70:73], v[210:213], v[202:205], v[70:73]
	v_mfma_i32_16x16x64_i8 v[66:69], v[218:221], v[202:205], v[66:69]
	ds_read_b128 v[202:205], v159 offset:39936
	s_setprio 0
	s_add_i32 s90, 0, 0x18000
	v_add_u32_e32 v154, s90, v157
	s_barrier
	ds_read_b128 v[146:149], v154
	ds_read_b128 v[150:153], v154 offset:1024
	ds_read_b128 v[164:167], v154 offset:2048
	ds_read_b128 v[168:171], v154 offset:3072
	s_add_u32 s68, s68, 0x40000
	s_addc_u32 s69, s69, 0
	s_waitcnt lgkmcnt(8)
	s_barrier
	s_setprio 1
	s_waitcnt lgkmcnt(0)
	v_mfma_i32_16x16x64_i8 v[62:65], v[146:149], v[172:175], v[62:65]
	s_mov_b32 m0, s54
	v_lshl_add_u64 v[206:207], s[68:69], 0, v[136:137]
	s_nop 0
	global_load_lds_dwordx4 v[206:207], off
	v_mfma_i32_16x16x64_i8 v[58:61], v[164:167], v[172:175], v[58:61]
	v_lshl_add_u64 v[206:207], s[68:69], 0, v[132:133]
	s_mov_b32 m0, s55
	s_nop 0
	global_load_lds_dwordx4 v[206:207], off
	v_mfma_i32_16x16x64_i8 v[54:57], v[146:149], v[180:183], v[54:57]
	v_mfma_i32_16x16x64_i8 v[50:53], v[164:167], v[180:183], v[50:53]
	v_mfma_i32_16x16x64_i8 v[46:49], v[146:149], v[188:191], v[46:49]
	v_mfma_i32_16x16x64_i8 v[42:45], v[164:167], v[188:191], v[42:45]
	v_mfma_i32_16x16x64_i8 v[38:41], v[146:149], v[198:201], v[38:41]
	v_mfma_i32_16x16x64_i8 v[34:37], v[164:167], v[198:201], v[34:37]
	v_mfma_i32_16x16x64_i8 v[62:65], v[150:153], v[176:179], v[62:65]
	v_mfma_i32_16x16x64_i8 v[58:61], v[168:171], v[176:179], v[58:61]
	v_mfma_i32_16x16x64_i8 v[54:57], v[150:153], v[184:187], v[54:57]
	v_mfma_i32_16x16x64_i8 v[50:53], v[168:171], v[184:187], v[50:53]
	v_mfma_i32_16x16x64_i8 v[46:49], v[150:153], v[192:195], v[46:49]
	v_mfma_i32_16x16x64_i8 v[42:45], v[168:171], v[192:195], v[42:45]
	v_mfma_i32_16x16x64_i8 v[38:41], v[150:153], v[202:205], v[38:41]
	v_mfma_i32_16x16x64_i8 v[34:37], v[168:171], v[202:205], v[34:37]
	s_setprio 0
	s_barrier
	s_add_i32 s68, 0, 0x1c000
	s_add_i32 s69, s90, s4
	v_add_u32_e32 v154, s68, v157
	ds_read_b128 v[206:209], v154
	ds_read_b128 v[210:213], v154 offset:1024
	ds_read_b128 v[214:217], v154 offset:2048
	ds_read_b128 v[218:221], v154 offset:3072
	s_barrier
	s_setprio 1
	s_waitcnt lgkmcnt(0)
	v_mfma_i32_16x16x64_i8 v[126:129], v[206:209], v[172:175], v[126:129]
	v_lshl_add_u64 v[222:223], v[222:223], 0, s[28:29]
	s_mov_b32 m0, s69
	s_nop 0
	global_load_lds_dwordx4 v[222:223], off
	v_mfma_i32_16x16x64_i8 v[122:125], v[214:217], v[172:175], v[122:125]
	v_lshl_add_u64 v[222:223], v[224:225], 0, s[28:29]
	s_add_i32 m0, s69, 0x2000
	s_nop 0
	global_load_lds_dwordx4 v[222:223], off
	ds_read_b128 v[172:175], v159 offset:49152
	v_mfma_i32_16x16x64_i8 v[118:121], v[206:209], v[180:183], v[118:121]
	v_mfma_i32_16x16x64_i8 v[114:117], v[214:217], v[180:183], v[114:117]
	ds_read_b128 v[180:183], v159 offset:51200
	v_mfma_i32_16x16x64_i8 v[110:113], v[206:209], v[188:191], v[110:113]
	v_mfma_i32_16x16x64_i8 v[106:109], v[214:217], v[188:191], v[106:109]
	ds_read_b128 v[188:191], v159 offset:53248
	v_mfma_i32_16x16x64_i8 v[102:105], v[206:209], v[198:201], v[102:105]
	v_mfma_i32_16x16x64_i8 v[98:101], v[214:217], v[198:201], v[98:101]
	ds_read_b128 v[198:201], v159 offset:55296
	v_mfma_i32_16x16x64_i8 v[126:129], v[210:213], v[176:179], v[126:129]
	v_mfma_i32_16x16x64_i8 v[122:125], v[218:221], v[176:179], v[122:125]
	ds_read_b128 v[176:179], v159 offset:50176
	v_mfma_i32_16x16x64_i8 v[118:121], v[210:213], v[184:187], v[118:121]
	v_mfma_i32_16x16x64_i8 v[114:117], v[218:221], v[184:187], v[114:117]
	ds_read_b128 v[184:187], v159 offset:52224
	v_mfma_i32_16x16x64_i8 v[110:113], v[210:213], v[192:195], v[110:113]
	v_mfma_i32_16x16x64_i8 v[106:109], v[218:221], v[192:195], v[106:109]
	ds_read_b128 v[192:195], v159 offset:54272
	v_mfma_i32_16x16x64_i8 v[102:105], v[210:213], v[202:205], v[102:105]
	v_mfma_i32_16x16x64_i8 v[98:101], v[218:221], v[202:205], v[98:101]
	ds_read_b128 v[202:205], v159 offset:56320
	s_setprio 0
	s_barrier
	s_barrier
	s_setprio 1
	s_waitcnt lgkmcnt(0)
	v_mfma_i32_16x16x64_i8 v[30:33], v[146:149], v[172:175], v[30:33]
	s_mov_b32 m0, s73
	v_lshl_add_u64 v[222:223], v[226:227], 0, s[28:29]
	s_nop 0
	global_load_lds_dwordx4 v[222:223], off
	v_mfma_i32_16x16x64_i8 v[26:29], v[164:167], v[172:175], v[26:29]
	v_lshl_add_u64 v[222:223], v[228:229], 0, s[28:29]
	s_mov_b32 m0, s74
	s_nop 0
	global_load_lds_dwordx4 v[222:223], off
	v_mfma_i32_16x16x64_i8 v[22:25], v[146:149], v[180:183], v[22:25]
	v_mfma_i32_16x16x64_i8 v[18:21], v[164:167], v[180:183], v[18:21]
	v_mfma_i32_16x16x64_i8 v[14:17], v[146:149], v[188:191], v[14:17]
	v_mfma_i32_16x16x64_i8 v[10:13], v[164:167], v[188:191], v[10:13]
	v_mfma_i32_16x16x64_i8 v[6:9], v[146:149], v[198:201], v[6:9]
	v_mfma_i32_16x16x64_i8 v[2:5], v[164:167], v[198:201], v[2:5]
	v_mfma_i32_16x16x64_i8 v[30:33], v[150:153], v[176:179], v[30:33]
	v_mfma_i32_16x16x64_i8 v[26:29], v[168:171], v[176:179], v[26:29]
	v_mfma_i32_16x16x64_i8 v[22:25], v[150:153], v[184:187], v[22:25]
	v_mfma_i32_16x16x64_i8 v[18:21], v[168:171], v[184:187], v[18:21]
	v_mfma_i32_16x16x64_i8 v[14:17], v[150:153], v[192:195], v[14:17]
	v_mfma_i32_16x16x64_i8 v[10:13], v[168:171], v[192:195], v[10:13]
	v_mfma_i32_16x16x64_i8 v[6:9], v[150:153], v[202:205], v[6:9]
	v_mfma_i32_16x16x64_i8 v[2:5], v[168:171], v[202:205], v[2:5]
	s_setprio 0
	s_barrier
	s_add_u32 s66, s66, 0x40080
	s_addc_u32 s67, s67, 0
	s_add_i32 s68, s68, s4
	v_lshl_add_u64 v[146:147], s[66:67], 0, v[134:135]
	s_mov_b32 m0, s68
	s_nop 0
	global_load_lds_dwordx4 v[146:147], off
	v_lshl_add_u64 v[146:147], s[66:67], 0, v[130:131]
	s_add_i32 m0, s68, 0x2000
	s_nop 0
	global_load_lds_dwordx4 v[146:147], off
	s_waitcnt vmcnt(6)
	s_barrier
	s_setprio 1
	v_mfma_i32_16x16x64_i8 v[94:97], v[206:209], v[172:175], v[94:97]
	v_add_u32_e32 v154, s77, v157
	ds_read_b128 v[146:149], v154
	ds_read_b128 v[150:153], v154 offset:1024
	ds_read_b128 v[164:167], v154 offset:2048
	ds_read_b128 v[168:171], v154 offset:3072
	v_mfma_i32_16x16x64_i8 v[90:93], v[214:217], v[172:175], v[90:93]
	ds_read_b128 v[172:175], v159
	v_mfma_i32_16x16x64_i8 v[86:89], v[206:209], v[180:183], v[86:89]
	v_mfma_i32_16x16x64_i8 v[82:85], v[214:217], v[180:183], v[82:85]
	ds_read_b128 v[180:183], v159 offset:2048
	v_mfma_i32_16x16x64_i8 v[78:81], v[206:209], v[188:191], v[78:81]
	v_mfma_i32_16x16x64_i8 v[74:77], v[214:217], v[188:191], v[74:77]
	ds_read_b128 v[188:191], v159 offset:4096
	v_mfma_i32_16x16x64_i8 v[70:73], v[206:209], v[198:201], v[70:73]
	v_mfma_i32_16x16x64_i8 v[66:69], v[214:217], v[198:201], v[66:69]
	ds_read_b128 v[198:201], v159 offset:6144
	v_mfma_i32_16x16x64_i8 v[94:97], v[210:213], v[176:179], v[94:97]
	v_mfma_i32_16x16x64_i8 v[90:93], v[218:221], v[176:179], v[90:93]
	ds_read_b128 v[176:179], v159 offset:1024
	v_mfma_i32_16x16x64_i8 v[86:89], v[210:213], v[184:187], v[86:89]
	v_mfma_i32_16x16x64_i8 v[82:85], v[218:221], v[184:187], v[82:85]
	ds_read_b128 v[184:187], v159 offset:3072
	v_mfma_i32_16x16x64_i8 v[78:81], v[210:213], v[192:195], v[78:81]
	v_mfma_i32_16x16x64_i8 v[74:77], v[218:221], v[192:195], v[74:77]
	ds_read_b128 v[192:195], v159 offset:5120
	v_mfma_i32_16x16x64_i8 v[70:73], v[210:213], v[202:205], v[70:73]
	v_mfma_i32_16x16x64_i8 v[66:69], v[218:221], v[202:205], v[66:69]
	ds_read_b128 v[202:205], v159 offset:7168
	s_setprio 0
	s_add_u32 s10, s10, 0x100
	s_addc_u32 s11, s11, 0
	s_add_u32 s87, s87, 0x100
	s_addc_u32 s88, s88, 0
	s_cmp_ge_i32 s89, s1
	s_mov_b32 s66, s89
	s_barrier
	s_cbranch_scc0 .LBB0_193
	s_branch .Lmy_pl0_exit
.LBB0_193:
	s_add_i32 s89, s66, 2
	s_add_u32 s67, s10, 0xfffc0080
	s_addc_u32 s68, s11, -1
	s_cmp_eq_u32 s75, s66
	s_cselect_b32 s66, s86, s87
	s_cselect_b32 s69, s9, s68
	s_cselect_b32 s68, s59, s67
	s_cselect_b32 s67, s61, s88
	v_lshl_add_u64 v[206:207], s[10:11], 0, v[138:139]
	s_add_i32 m0, s52, 0xc000
	global_load_lds_dwordx4 v[206:207], off
	v_lshl_add_u64 v[206:207], s[10:11], 0, v[140:141]
	s_add_i32 m0, s52, 0xe000
	s_nop 0
	global_load_lds_dwordx4 v[206:207], off
	s_waitcnt lgkmcnt(8)
	s_barrier
	s_setprio 1
	s_waitcnt lgkmcnt(0)
	v_mfma_i32_16x16x64_i8 v[62:65], v[146:149], v[172:175], v[62:65]
	v_mfma_i32_16x16x64_i8 v[58:61], v[164:167], v[172:175], v[58:61]
	v_mfma_i32_16x16x64_i8 v[54:57], v[146:149], v[180:183], v[54:57]
	v_mfma_i32_16x16x64_i8 v[50:53], v[164:167], v[180:183], v[50:53]
	v_mfma_i32_16x16x64_i8 v[46:49], v[146:149], v[188:191], v[46:49]
	v_mfma_i32_16x16x64_i8 v[42:45], v[164:167], v[188:191], v[42:45]
	v_mfma_i32_16x16x64_i8 v[38:41], v[146:149], v[198:201], v[38:41]
	v_mfma_i32_16x16x64_i8 v[34:37], v[164:167], v[198:201], v[34:37]
	v_mfma_i32_16x16x64_i8 v[62:65], v[150:153], v[176:179], v[62:65]
	v_mfma_i32_16x16x64_i8 v[58:61], v[168:171], v[176:179], v[58:61]
	v_mfma_i32_16x16x64_i8 v[54:57], v[150:153], v[184:187], v[54:57]
	v_mfma_i32_16x16x64_i8 v[50:53], v[168:171], v[184:187], v[50:53]
	v_mfma_i32_16x16x64_i8 v[46:49], v[150:153], v[192:195], v[46:49]
	v_mfma_i32_16x16x64_i8 v[42:45], v[168:171], v[192:195], v[42:45]
	v_mfma_i32_16x16x64_i8 v[38:41], v[150:153], v[202:205], v[38:41]
	v_mfma_i32_16x16x64_i8 v[34:37], v[168:171], v[202:205], v[34:37]
	s_setprio 0
	s_barrier
	s_add_i32 s90, s77, s4
	v_add_u32_e32 v154, s78, v157
	ds_read_b128 v[206:209], v154
	ds_read_b128 v[210:213], v154 offset:1024
	ds_read_b128 v[214:217], v154 offset:2048
	ds_read_b128 v[218:221], v154 offset:3072
	s_barrier
	s_setprio 1
	s_waitcnt lgkmcnt(0)
	v_mfma_i32_16x16x64_i8 v[126:129], v[206:209], v[172:175], v[126:129]
	v_lshl_add_u64 v[222:223], s[66:67], 0, v[134:135]
	s_mov_b32 m0, s90
	s_nop 0
	global_load_lds_dwordx4 v[222:223], off
	v_mfma_i32_16x16x64_i8 v[122:125], v[214:217], v[172:175], v[122:125]
	v_lshl_add_u64 v[224:225], s[66:67], 0, v[130:131]
	s_add_i32 m0, s90, 0x2000
	s_nop 0
	global_load_lds_dwordx4 v[224:225], off
	ds_read_b128 v[172:175], v159 offset:16384
	v_mfma_i32_16x16x64_i8 v[118:121], v[206:209], v[180:183], v[118:121]
	v_mfma_i32_16x16x64_i8 v[114:117], v[214:217], v[180:183], v[114:117]
	ds_read_b128 v[180:183], v159 offset:18432
	v_mfma_i32_16x16x64_i8 v[110:113], v[206:209], v[188:191], v[110:113]
	v_mfma_i32_16x16x64_i8 v[106:109], v[214:217], v[188:191], v[106:109]
	ds_read_b128 v[188:191], v159 offset:20480
	v_mfma_i32_16x16x64_i8 v[102:105], v[206:209], v[198:201], v[102:105]
	v_mfma_i32_16x16x64_i8 v[98:101], v[214:217], v[198:201], v[98:101]
	ds_read_b128 v[198:201], v159 offset:22528
	v_mfma_i32_16x16x64_i8 v[126:129], v[210:213], v[176:179], v[126:129]
	v_mfma_i32_16x16x64_i8 v[122:125], v[218:221], v[176:179], v[122:125]
	ds_read_b128 v[176:179], v159 offset:17408
	v_mfma_i32_16x16x64_i8 v[118:121], v[210:213], v[184:187], v[118:121]
	v_mfma_i32_16x16x64_i8 v[114:117], v[218:221], v[184:187], v[114:117]
	ds_read_b128 v[184:187], v159 offset:19456
	v_mfma_i32_16x16x64_i8 v[110:113], v[210:213], v[192:195], v[110:113]
	v_mfma_i32_16x16x64_i8 v[106:109], v[218:221], v[192:195], v[106:109]
	ds_read_b128 v[192:195], v159 offset:21504
	v_mfma_i32_16x16x64_i8 v[102:105], v[210:213], v[202:205], v[102:105]
	v_mfma_i32_16x16x64_i8 v[98:101], v[218:221], v[202:205], v[98:101]
	ds_read_b128 v[202:205], v159 offset:23552
	s_setprio 0
	s_barrier
	s_barrier
	s_setprio 1
	s_waitcnt lgkmcnt(0)
	v_mfma_i32_16x16x64_i8 v[30:33], v[146:149], v[172:175], v[30:33]
	s_mov_b32 m0, s52
	v_lshl_add_u64 v[226:227], s[68:69], 0, v[136:137]
	s_nop 0
	global_load_lds_dwordx4 v[226:227], off
	v_mfma_i32_16x16x64_i8 v[26:29], v[164:167], v[172:175], v[26:29]
	v_lshl_add_u64 v[228:229], s[68:69], 0, v[132:133]
	s_mov_b32 m0, s53
	s_nop 0
	global_load_lds_dwordx4 v[228:229], off
	v_mfma_i32_16x16x64_i8 v[22:25], v[146:149], v[180:183], v[22:25]
	v_mfma_i32_16x16x64_i8 v[18:21], v[164:167], v[180:183], v[18:21]
	v_mfma_i32_16x16x64_i8 v[14:17], v[146:149], v[188:191], v[14:17]
	v_mfma_i32_16x16x64_i8 v[10:13], v[164:167], v[188:191], v[10:13]
	v_mfma_i32_16x16x64_i8 v[6:9], v[146:149], v[198:201], v[6:9]
	v_mfma_i32_16x16x64_i8 v[2:5], v[164:167], v[198:201], v[2:5]
	v_mfma_i32_16x16x64_i8 v[30:33], v[150:153], v[176:179], v[30:33]
	v_mfma_i32_16x16x64_i8 v[26:29], v[168:171], v[176:179], v[26:29]
	v_mfma_i32_16x16x64_i8 v[22:25], v[150:153], v[184:187], v[22:25]
	v_mfma_i32_16x16x64_i8 v[18:21], v[168:171], v[184:187], v[18:21]
	v_mfma_i32_16x16x64_i8 v[14:17], v[150:153], v[192:195], v[14:17]
	v_mfma_i32_16x16x64_i8 v[10:13], v[168:171], v[192:195], v[10:13]
	v_mfma_i32_16x16x64_i8 v[6:9], v[150:153], v[202:205], v[6:9]
	v_mfma_i32_16x16x64_i8 v[2:5], v[168:171], v[202:205], v[2:5]
	s_setprio 0
	s_barrier
	s_add_u32 s90, s66, 0x40000
	s_addc_u32 s91, s67, 0
	s_add_i32 s92, s78, s4
	v_lshl_add_u64 v[146:147], s[90:91], 0, v[134:135]
	s_mov_b32 m0, s92
	s_nop 0
	global_load_lds_dwordx4 v[146:147], off
	v_lshl_add_u64 v[146:147], s[90:91], 0, v[130:131]
	s_add_i32 m0, s92, 0x2000
	s_nop 0
	global_load_lds_dwordx4 v[146:147], off
	s_waitcnt vmcnt(6)
	s_barrier
	s_setprio 1
	v_mfma_i32_16x16x64_i8 v[94:97], v[206:209], v[172:175], v[94:97]
	v_mfma_i32_16x16x64_i8 v[90:93], v[214:217], v[172:175], v[90:93]
	ds_read_b128 v[172:175], v159 offset:32768
	v_mfma_i32_16x16x64_i8 v[86:89], v[206:209], v[180:183], v[86:89]
	v_mfma_i32_16x16x64_i8 v[82:85], v[214:217], v[180:183], v[82:85]
	ds_read_b128 v[180:183], v159 offset:34816
	v_mfma_i32_16x16x64_i8 v[78:81], v[206:209], v[188:191], v[78:81]
	v_mfma_i32_16x16x64_i8 v[74:77], v[214:217], v[188:191], v[74:77]
	ds_read_b128 v[188:191], v159 offset:36864
	v_mfma_i32_16x16x64_i8 v[70:73], v[206:209], v[198:201], v[70:73]
	v_mfma_i32_16x16x64_i8 v[66:69], v[214:217], v[198:201], v[66:69]
	ds_read_b128 v[198:201], v159 offset:38912
	v_mfma_i32_16x16x64_i8 v[94:97], v[210:213], v[176:179], v[94:97]
	v_mfma_i32_16x16x64_i8 v[90:93], v[218:221], v[176:179], v[90:93]
	ds_read_b128 v[176:179], v159 offset:33792
	v_mfma_i32_16x16x64_i8 v[86:89], v[210:213], v[184:187], v[86:89]
	v_mfma_i32_16x16x64_i8 v[82:85], v[218:221], v[184:187], v[82:85]
	ds_read_b128 v[184:187], v159 offset:35840
	v_mfma_i32_16x16x64_i8 v[78:81], v[210:213], v[192:195], v[78:81]
	v_mfma_i32_16x16x64_i8 v[74:77], v[218:221], v[192:195], v[74:77]
	ds_read_b128 v[192:195], v159 offset:37888
	v_mfma_i32_16x16x64_i8 v[70:73], v[210:213], v[202:205], v[70:73]
	v_mfma_i32_16x16x64_i8 v[66:69], v[218:221], v[202:205], v[66:69]
	ds_read_b128 v[202:205], v159 offset:39936
	s_setprio 0
	s_add_i32 s90, 0, 0x18000
	v_add_u32_e32 v154, s90, v157
	s_barrier
	ds_read_b128 v[146:149], v154
	ds_read_b128 v[150:153], v154 offset:1024
	ds_read_b128 v[164:167], v154 offset:2048
	ds_read_b128 v[168:171], v154 offset:3072
	s_add_u32 s68, s68, 0x40000
	s_addc_u32 s69, s69, 0
	s_waitcnt lgkmcnt(8)
	s_barrier
	s_setprio 1
	s_waitcnt lgkmcnt(0)
	v_mfma_i32_16x16x64_i8 v[62:65], v[146:149], v[172:175], v[62:65]
	s_mov_b32 m0, s54
	v_lshl_add_u64 v[206:207], s[68:69], 0, v[136:137]
	s_nop 0
	global_load_lds_dwordx4 v[206:207], off
	v_mfma_i32_16x16x64_i8 v[58:61], v[164:167], v[172:175], v[58:61]
	v_lshl_add_u64 v[206:207], s[68:69], 0, v[132:133]
	s_mov_b32 m0, s55
	s_nop 0
	global_load_lds_dwordx4 v[206:207], off
	v_mfma_i32_16x16x64_i8 v[54:57], v[146:149], v[180:183], v[54:57]
	v_mfma_i32_16x16x64_i8 v[50:53], v[164:167], v[180:183], v[50:53]
	v_mfma_i32_16x16x64_i8 v[46:49], v[146:149], v[188:191], v[46:49]
	v_mfma_i32_16x16x64_i8 v[42:45], v[164:167], v[188:191], v[42:45]
	v_mfma_i32_16x16x64_i8 v[38:41], v[146:149], v[198:201], v[38:41]
	v_mfma_i32_16x16x64_i8 v[34:37], v[164:167], v[198:201], v[34:37]
	v_mfma_i32_16x16x64_i8 v[62:65], v[150:153], v[176:179], v[62:65]
	v_mfma_i32_16x16x64_i8 v[58:61], v[168:171], v[176:179], v[58:61]
	v_mfma_i32_16x16x64_i8 v[54:57], v[150:153], v[184:187], v[54:57]
	v_mfma_i32_16x16x64_i8 v[50:53], v[168:171], v[184:187], v[50:53]
	v_mfma_i32_16x16x64_i8 v[46:49], v[150:153], v[192:195], v[46:49]
	v_mfma_i32_16x16x64_i8 v[42:45], v[168:171], v[192:195], v[42:45]
	v_mfma_i32_16x16x64_i8 v[38:41], v[150:153], v[202:205], v[38:41]
	v_mfma_i32_16x16x64_i8 v[34:37], v[168:171], v[202:205], v[34:37]
	s_setprio 0
	s_barrier
	s_add_i32 s68, 0, 0x1c000
	s_add_i32 s69, s90, s4
	v_add_u32_e32 v154, s68, v157
	ds_read_b128 v[206:209], v154
	ds_read_b128 v[210:213], v154 offset:1024
	ds_read_b128 v[214:217], v154 offset:2048
	ds_read_b128 v[218:221], v154 offset:3072
	s_barrier
	s_setprio 1
	s_waitcnt lgkmcnt(0)
	v_mfma_i32_16x16x64_i8 v[126:129], v[206:209], v[172:175], v[126:129]
	v_lshl_add_u64 v[222:223], v[222:223], 0, s[28:29]
	s_mov_b32 m0, s69
	s_nop 0
	global_load_lds_dwordx4 v[222:223], off
	v_mfma_i32_16x16x64_i8 v[122:125], v[214:217], v[172:175], v[122:125]
	v_lshl_add_u64 v[222:223], v[224:225], 0, s[28:29]
	s_add_i32 m0, s69, 0x2000
	s_nop 0
	global_load_lds_dwordx4 v[222:223], off
	ds_read_b128 v[172:175], v159 offset:49152
	v_mfma_i32_16x16x64_i8 v[118:121], v[206:209], v[180:183], v[118:121]
	v_mfma_i32_16x16x64_i8 v[114:117], v[214:217], v[180:183], v[114:117]
	ds_read_b128 v[180:183], v159 offset:51200
	v_mfma_i32_16x16x64_i8 v[110:113], v[206:209], v[188:191], v[110:113]
	v_mfma_i32_16x16x64_i8 v[106:109], v[214:217], v[188:191], v[106:109]
	ds_read_b128 v[188:191], v159 offset:53248
	v_mfma_i32_16x16x64_i8 v[102:105], v[206:209], v[198:201], v[102:105]
	v_mfma_i32_16x16x64_i8 v[98:101], v[214:217], v[198:201], v[98:101]
	ds_read_b128 v[198:201], v159 offset:55296
	v_mfma_i32_16x16x64_i8 v[126:129], v[210:213], v[176:179], v[126:129]
	v_mfma_i32_16x16x64_i8 v[122:125], v[218:221], v[176:179], v[122:125]
	ds_read_b128 v[176:179], v159 offset:50176
	v_mfma_i32_16x16x64_i8 v[118:121], v[210:213], v[184:187], v[118:121]
	v_mfma_i32_16x16x64_i8 v[114:117], v[218:221], v[184:187], v[114:117]
	ds_read_b128 v[184:187], v159 offset:52224
	v_mfma_i32_16x16x64_i8 v[110:113], v[210:213], v[192:195], v[110:113]
	v_mfma_i32_16x16x64_i8 v[106:109], v[218:221], v[192:195], v[106:109]
	ds_read_b128 v[192:195], v159 offset:54272
	v_mfma_i32_16x16x64_i8 v[102:105], v[210:213], v[202:205], v[102:105]
	v_mfma_i32_16x16x64_i8 v[98:101], v[218:221], v[202:205], v[98:101]
	ds_read_b128 v[202:205], v159 offset:56320
	s_setprio 0
	s_barrier
	s_barrier
	s_setprio 1
	s_waitcnt lgkmcnt(0)
	v_mfma_i32_16x16x64_i8 v[30:33], v[146:149], v[172:175], v[30:33]
	s_mov_b32 m0, s73
	v_lshl_add_u64 v[222:223], v[226:227], 0, s[28:29]
	s_nop 0
	global_load_lds_dwordx4 v[222:223], off
	v_mfma_i32_16x16x64_i8 v[26:29], v[164:167], v[172:175], v[26:29]
	v_lshl_add_u64 v[222:223], v[228:229], 0, s[28:29]
	s_mov_b32 m0, s74
	s_nop 0
	global_load_lds_dwordx4 v[222:223], off
	v_mfma_i32_16x16x64_i8 v[22:25], v[146:149], v[180:183], v[22:25]
	v_mfma_i32_16x16x64_i8 v[18:21], v[164:167], v[180:183], v[18:21]
	v_mfma_i32_16x16x64_i8 v[14:17], v[146:149], v[188:191], v[14:17]
	v_mfma_i32_16x16x64_i8 v[10:13], v[164:167], v[188:191], v[10:13]
	v_mfma_i32_16x16x64_i8 v[6:9], v[146:149], v[198:201], v[6:9]
	v_mfma_i32_16x16x64_i8 v[2:5], v[164:167], v[198:201], v[2:5]
	v_mfma_i32_16x16x64_i8 v[30:33], v[150:153], v[176:179], v[30:33]
	v_mfma_i32_16x16x64_i8 v[26:29], v[168:171], v[176:179], v[26:29]
	v_mfma_i32_16x16x64_i8 v[22:25], v[150:153], v[184:187], v[22:25]
	v_mfma_i32_16x16x64_i8 v[18:21], v[168:171], v[184:187], v[18:21]
	v_mfma_i32_16x16x64_i8 v[14:17], v[150:153], v[192:195], v[14:17]
	v_mfma_i32_16x16x64_i8 v[10:13], v[168:171], v[192:195], v[10:13]
	v_mfma_i32_16x16x64_i8 v[6:9], v[150:153], v[202:205], v[6:9]
	v_mfma_i32_16x16x64_i8 v[2:5], v[168:171], v[202:205], v[2:5]
	s_setprio 0
	s_barrier
	s_add_u32 s66, s66, 0x40080
	s_addc_u32 s67, s67, 0
	s_add_i32 s68, s68, s4
	v_lshl_add_u64 v[146:147], s[66:67], 0, v[134:135]
	s_mov_b32 m0, s68
	s_nop 0
	global_load_lds_dwordx4 v[146:147], off
	v_lshl_add_u64 v[146:147], s[66:67], 0, v[130:131]
	s_add_i32 m0, s68, 0x2000
	s_nop 0
	global_load_lds_dwordx4 v[146:147], off
	s_waitcnt vmcnt(6)
	s_barrier
	s_setprio 1
	v_mfma_i32_16x16x64_i8 v[94:97], v[206:209], v[172:175], v[94:97]
	v_add_u32_e32 v154, s77, v157
	ds_read_b128 v[146:149], v154
	ds_read_b128 v[150:153], v154 offset:1024
	ds_read_b128 v[164:167], v154 offset:2048
	ds_read_b128 v[168:171], v154 offset:3072
	v_mfma_i32_16x16x64_i8 v[90:93], v[214:217], v[172:175], v[90:93]
	ds_read_b128 v[172:175], v159
	v_mfma_i32_16x16x64_i8 v[86:89], v[206:209], v[180:183], v[86:89]
	v_mfma_i32_16x16x64_i8 v[82:85], v[214:217], v[180:183], v[82:85]
	ds_read_b128 v[180:183], v159 offset:2048
	v_mfma_i32_16x16x64_i8 v[78:81], v[206:209], v[188:191], v[78:81]
	v_mfma_i32_16x16x64_i8 v[74:77], v[214:217], v[188:191], v[74:77]
	ds_read_b128 v[188:191], v159 offset:4096
	v_mfma_i32_16x16x64_i8 v[70:73], v[206:209], v[198:201], v[70:73]
	v_mfma_i32_16x16x64_i8 v[66:69], v[214:217], v[198:201], v[66:69]
	ds_read_b128 v[198:201], v159 offset:6144
	v_mfma_i32_16x16x64_i8 v[94:97], v[210:213], v[176:179], v[94:97]
	v_mfma_i32_16x16x64_i8 v[90:93], v[218:221], v[176:179], v[90:93]
	ds_read_b128 v[176:179], v159 offset:1024
	v_mfma_i32_16x16x64_i8 v[86:89], v[210:213], v[184:187], v[86:89]
	v_mfma_i32_16x16x64_i8 v[82:85], v[218:221], v[184:187], v[82:85]
	ds_read_b128 v[184:187], v159 offset:3072
	v_mfma_i32_16x16x64_i8 v[78:81], v[210:213], v[192:195], v[78:81]
	v_mfma_i32_16x16x64_i8 v[74:77], v[218:221], v[192:195], v[74:77]
	ds_read_b128 v[192:195], v159 offset:5120
	v_mfma_i32_16x16x64_i8 v[70:73], v[210:213], v[202:205], v[70:73]
	v_mfma_i32_16x16x64_i8 v[66:69], v[218:221], v[202:205], v[66:69]
	ds_read_b128 v[202:205], v159 offset:7168
	s_setprio 0
	s_add_u32 s10, s10, 0x100
	s_addc_u32 s11, s11, 0
	s_add_u32 s87, s87, 0x100
	s_addc_u32 s88, s88, 0
	s_cmp_ge_i32 s89, s1
	s_mov_b32 s66, s89
	s_barrier
	s_cbranch_scc0 .LBB0_193

.LBB0_962:
	s_ashr_i32 s27, s26, 31
	s_lshl_b64 s[28:29], s[26:27], 20
	s_add_u32 s28, s10, s28
	s_addc_u32 s29, s11, s29
	s_ashr_i32 s25, s24, 31
	s_lshl_b64 s[30:31], s[24:25], 20
	s_add_u32 s30, s14, s30
	v_cmp_lt_i64_e64 s[8:9], s[8:9], v[158:159]
	s_addc_u32 s31, s15, s31
	s_andn2_b64 vcc, exec, s[20:21]
	s_cbranch_vccnz .LBB0_954
	s_and_b64 s[8:9], s[8:9], exec
	s_cselect_b32 s25, s29, s39
	s_cselect_b32 s27, s28, s38
	s_cselect_b32 s51, s31, s37
	s_cselect_b32 s52, s30, s36
	s_add_u32 s8, s38, 0x80080
	s_addc_u32 s9, s39, 0
	s_add_u32 s53, s36, 0x100
	v_mov_b32_e32 v2, 0
	s_addc_u32 s54, s37, 0
	s_mov_b32 s36, 0
	ds_read_b128 v[130:133], v172
	ds_read_b128 v[134:137], v172 offset:1024
	ds_read_b128 v[138:141], v172 offset:2048
	ds_read_b128 v[142:145], v172 offset:3072
	s_add_i32 s55, s36, 2
	s_add_u32 s37, s8, 0xfff80080
	s_addc_u32 s38, s9, -1
	s_cmp_eq_u32 s46, s36
	s_cselect_b32 s36, s52, s53
	s_cselect_b32 s39, s25, s38
	s_cselect_b32 s38, s27, s37
	s_cselect_b32 s37, s51, s54
	v_lshl_add_u64 v[200:201], s[8:9], 0, v[154:155]
	s_add_i32 m0, s23, 0xc000
	ds_read_b128 v[162:165], v173
	ds_read_b128 v[166:169], v173 offset:1024
	ds_read_b128 v[176:179], v173 offset:2048
	ds_read_b128 v[180:183], v173 offset:3072
	ds_read_b128 v[184:187], v173 offset:4096
	ds_read_b128 v[188:191], v173 offset:5120
	ds_read_b128 v[192:195], v173 offset:6144
	ds_read_b128 v[196:199], v173 offset:7168
	global_load_lds_dwordx4 v[200:201], off
	v_lshl_add_u64 v[200:201], s[8:9], 0, v[156:157]
	s_add_i32 m0, s23, 0xe000
	s_nop 0
	global_load_lds_dwordx4 v[200:201], off
	s_waitcnt lgkmcnt(8)
	s_barrier
	s_setprio 1
	s_waitcnt lgkmcnt(0)
	v_mfma_f32_16x16x32_bf16 v[126:129], v[130:133], v[162:165], 0
	ds_read_b128 v[200:203], v174
	ds_read_b128 v[204:207], v174 offset:1024
	ds_read_b128 v[208:211], v174 offset:2048
	ds_read_b128 v[214:217], v174 offset:3072
	v_mfma_f32_16x16x32_bf16 v[122:125], v[138:141], v[162:165], 0
	v_mfma_f32_16x16x32_bf16 v[110:113], v[130:133], v[176:179], 0
	v_mfma_f32_16x16x32_bf16 v[106:109], v[138:141], v[176:179], 0
	v_mfma_f32_16x16x32_bf16 v[94:97], v[130:133], v[184:187], 0
	v_mfma_f32_16x16x32_bf16 v[90:93], v[138:141], v[184:187], 0
	v_mfma_f32_16x16x32_bf16 v[78:81], v[130:133], v[192:195], 0
	v_mfma_f32_16x16x32_bf16 v[74:77], v[138:141], v[192:195], 0
	v_mfma_f32_16x16x32_bf16 v[126:129], v[134:137], v[166:169], v[126:129]
	v_mfma_f32_16x16x32_bf16 v[122:125], v[142:145], v[166:169], v[122:125]
	v_mfma_f32_16x16x32_bf16 v[110:113], v[134:137], v[180:183], v[110:113]
	v_mfma_f32_16x16x32_bf16 v[106:109], v[142:145], v[180:183], v[106:109]
	v_mfma_f32_16x16x32_bf16 v[94:97], v[134:137], v[188:191], v[94:97]
	v_mfma_f32_16x16x32_bf16 v[90:93], v[142:145], v[188:191], v[90:93]
	v_mfma_f32_16x16x32_bf16 v[78:81], v[134:137], v[196:199], v[78:81]
	v_mfma_f32_16x16x32_bf16 v[74:77], v[142:145], v[196:199], v[74:77]
	s_setprio 0
	s_barrier
	s_add_i32 s56, s48, s5
	s_barrier
	s_setprio 1
	s_waitcnt lgkmcnt(0)
	v_mfma_f32_16x16x32_bf16 v[118:121], v[200:203], v[162:165], 0
	v_lshl_add_u64 v[218:219], s[36:37], 0, v[148:149]
	s_mov_b32 m0, s56
	s_nop 0
	global_load_lds_dwordx4 v[218:219], off
	v_mfma_f32_16x16x32_bf16 v[114:117], v[208:211], v[162:165], 0
	v_lshl_add_u64 v[220:221], s[36:37], 0, v[152:153]
	s_add_i32 m0, s56, 0x2000
	s_nop 0
	global_load_lds_dwordx4 v[220:221], off
	ds_read_b128 v[162:165], v173 offset:16384
	v_mfma_f32_16x16x32_bf16 v[102:105], v[200:203], v[176:179], 0
	v_mfma_f32_16x16x32_bf16 v[98:101], v[208:211], v[176:179], 0
	ds_read_b128 v[176:179], v173 offset:18432
	v_mfma_f32_16x16x32_bf16 v[86:89], v[200:203], v[184:187], 0
	v_mfma_f32_16x16x32_bf16 v[82:85], v[208:211], v[184:187], 0
	ds_read_b128 v[184:187], v173 offset:20480
	v_mfma_f32_16x16x32_bf16 v[70:73], v[200:203], v[192:195], 0
	v_mfma_f32_16x16x32_bf16 v[66:69], v[208:211], v[192:195], 0
	ds_read_b128 v[192:195], v173 offset:22528
	v_mfma_f32_16x16x32_bf16 v[118:121], v[204:207], v[166:169], v[118:121]
	v_mfma_f32_16x16x32_bf16 v[114:117], v[214:217], v[166:169], v[114:117]
	ds_read_b128 v[166:169], v173 offset:17408
	v_mfma_f32_16x16x32_bf16 v[102:105], v[204:207], v[180:183], v[102:105]
	v_mfma_f32_16x16x32_bf16 v[98:101], v[214:217], v[180:183], v[98:101]
	ds_read_b128 v[180:183], v173 offset:19456
	v_mfma_f32_16x16x32_bf16 v[86:89], v[204:207], v[188:191], v[86:89]
	v_mfma_f32_16x16x32_bf16 v[82:85], v[214:217], v[188:191], v[82:85]
	ds_read_b128 v[188:191], v173 offset:21504
	v_mfma_f32_16x16x32_bf16 v[70:73], v[204:207], v[196:199], v[70:73]
	v_mfma_f32_16x16x32_bf16 v[66:69], v[214:217], v[196:199], v[66:69]
	ds_read_b128 v[196:199], v173 offset:23552
	s_setprio 0
	s_barrier
	s_barrier
	s_setprio 1
	s_waitcnt lgkmcnt(0)
	v_mfma_f32_16x16x32_bf16 v[62:65], v[130:133], v[162:165], 0
	s_mov_b32 m0, s23
	v_lshl_add_u64 v[222:223], s[38:39], 0, v[146:147]
	s_nop 0
	global_load_lds_dwordx4 v[222:223], off
	v_mfma_f32_16x16x32_bf16 v[58:61], v[138:141], v[162:165], 0
	v_lshl_add_u64 v[224:225], s[38:39], 0, v[150:151]
	s_mov_b32 m0, s33
	s_nop 0
	global_load_lds_dwordx4 v[224:225], off
	v_mfma_f32_16x16x32_bf16 v[46:49], v[130:133], v[176:179], 0
	v_mfma_f32_16x16x32_bf16 v[42:45], v[138:141], v[176:179], 0
	v_mfma_f32_16x16x32_bf16 v[30:33], v[130:133], v[184:187], 0
	v_mfma_f32_16x16x32_bf16 v[26:29], v[138:141], v[184:187], 0
	v_mfma_f32_16x16x32_bf16 v[14:17], v[130:133], v[192:195], 0
	v_mfma_f32_16x16x32_bf16 v[10:13], v[138:141], v[192:195], 0
	v_mfma_f32_16x16x32_bf16 v[62:65], v[134:137], v[166:169], v[62:65]
	v_mfma_f32_16x16x32_bf16 v[58:61], v[142:145], v[166:169], v[58:61]
	v_mfma_f32_16x16x32_bf16 v[46:49], v[134:137], v[180:183], v[46:49]
	v_mfma_f32_16x16x32_bf16 v[42:45], v[142:145], v[180:183], v[42:45]
	v_mfma_f32_16x16x32_bf16 v[30:33], v[134:137], v[188:191], v[30:33]
	v_mfma_f32_16x16x32_bf16 v[26:29], v[142:145], v[188:191], v[26:29]
	v_mfma_f32_16x16x32_bf16 v[14:17], v[134:137], v[196:199], v[14:17]
	v_mfma_f32_16x16x32_bf16 v[10:13], v[142:145], v[196:199], v[10:13]
	s_setprio 0
	s_barrier
	s_add_u32 s56, s36, 0x80000
	s_addc_u32 s57, s37, 0
	s_add_i32 s58, s49, s5
	v_lshl_add_u64 v[130:131], s[56:57], 0, v[148:149]
	s_mov_b32 m0, s58
	s_nop 0
	global_load_lds_dwordx4 v[130:131], off
	v_lshl_add_u64 v[130:131], s[56:57], 0, v[152:153]
	s_add_i32 m0, s58, 0x2000
	s_nop 0
	global_load_lds_dwordx4 v[130:131], off
	s_waitcnt vmcnt(6)
	s_barrier
	s_setprio 1
	v_mfma_f32_16x16x32_bf16 v[54:57], v[200:203], v[162:165], 0
	v_mfma_f32_16x16x32_bf16 v[50:53], v[208:211], v[162:165], 0
	ds_read_b128 v[162:165], v173 offset:32768
	v_mfma_f32_16x16x32_bf16 v[38:41], v[200:203], v[176:179], 0
	v_mfma_f32_16x16x32_bf16 v[34:37], v[208:211], v[176:179], 0
	ds_read_b128 v[176:179], v173 offset:34816
	v_mfma_f32_16x16x32_bf16 v[22:25], v[200:203], v[184:187], 0
	v_mfma_f32_16x16x32_bf16 v[18:21], v[208:211], v[184:187], 0
	ds_read_b128 v[184:187], v173 offset:36864
	v_mfma_f32_16x16x32_bf16 v[6:9], v[200:203], v[192:195], 0
	v_mfma_f32_16x16x32_bf16 v[2:5], v[208:211], v[192:195], 0
	ds_read_b128 v[192:195], v173 offset:38912
	v_mfma_f32_16x16x32_bf16 v[54:57], v[204:207], v[166:169], v[54:57]
	v_mfma_f32_16x16x32_bf16 v[50:53], v[214:217], v[166:169], v[50:53]
	ds_read_b128 v[166:169], v173 offset:33792
	v_mfma_f32_16x16x32_bf16 v[38:41], v[204:207], v[180:183], v[38:41]
	v_mfma_f32_16x16x32_bf16 v[34:37], v[214:217], v[180:183], v[34:37]
	ds_read_b128 v[180:183], v173 offset:35840
	v_mfma_f32_16x16x32_bf16 v[22:25], v[204:207], v[188:191], v[22:25]
	v_mfma_f32_16x16x32_bf16 v[18:21], v[214:217], v[188:191], v[18:21]
	ds_read_b128 v[188:191], v173 offset:37888
	v_mfma_f32_16x16x32_bf16 v[6:9], v[204:207], v[196:199], v[6:9]
	v_mfma_f32_16x16x32_bf16 v[2:5], v[214:217], v[196:199], v[2:5]
	ds_read_b128 v[196:199], v173 offset:39936
	s_setprio 0
	s_add_i32 s56, 0, 0x18000
	v_add_u32_e32 v142, s56, v171
	s_barrier
	ds_read_b128 v[130:133], v142
	ds_read_b128 v[134:137], v142 offset:1024
	ds_read_b128 v[138:141], v142 offset:2048
	ds_read_b128 v[142:145], v142 offset:3072
	s_add_u32 s38, s38, 0x80000
	s_addc_u32 s39, s39, 0
	s_waitcnt lgkmcnt(8)
	s_barrier
	s_setprio 1
	s_waitcnt lgkmcnt(0)
	v_mfma_f32_16x16x32_bf16 v[126:129], v[130:133], v[162:165], v[126:129]
	s_mov_b32 m0, s35
	v_lshl_add_u64 v[200:201], s[38:39], 0, v[146:147]
	s_nop 0
	global_load_lds_dwordx4 v[200:201], off
	v_mfma_f32_16x16x32_bf16 v[122:125], v[138:141], v[162:165], v[122:125]
	v_lshl_add_u64 v[200:201], s[38:39], 0, v[150:151]
	s_mov_b32 m0, s40
	s_nop 0
	global_load_lds_dwordx4 v[200:201], off
	v_mfma_f32_16x16x32_bf16 v[110:113], v[130:133], v[176:179], v[110:113]
	v_mfma_f32_16x16x32_bf16 v[106:109], v[138:141], v[176:179], v[106:109]
	v_mfma_f32_16x16x32_bf16 v[94:97], v[130:133], v[184:187], v[94:97]
	v_mfma_f32_16x16x32_bf16 v[90:93], v[138:141], v[184:187], v[90:93]
	v_mfma_f32_16x16x32_bf16 v[78:81], v[130:133], v[192:195], v[78:81]
	v_mfma_f32_16x16x32_bf16 v[74:77], v[138:141], v[192:195], v[74:77]
	v_mfma_f32_16x16x32_bf16 v[126:129], v[134:137], v[166:169], v[126:129]
	v_mfma_f32_16x16x32_bf16 v[122:125], v[142:145], v[166:169], v[122:125]
	v_mfma_f32_16x16x32_bf16 v[110:113], v[134:137], v[180:183], v[110:113]
	v_mfma_f32_16x16x32_bf16 v[106:109], v[142:145], v[180:183], v[106:109]
	v_mfma_f32_16x16x32_bf16 v[94:97], v[134:137], v[188:191], v[94:97]
	v_mfma_f32_16x16x32_bf16 v[90:93], v[142:145], v[188:191], v[90:93]
	v_mfma_f32_16x16x32_bf16 v[78:81], v[134:137], v[196:199], v[78:81]
	v_mfma_f32_16x16x32_bf16 v[74:77], v[142:145], v[196:199], v[74:77]
	s_setprio 0
	s_barrier
	s_add_i32 s38, 0, 0x1c000
	s_add_i32 s39, s56, s5
	v_add_u32_e32 v175, s38, v171
	ds_read_b128 v[200:203], v175
	ds_read_b128 v[204:207], v175 offset:1024
	ds_read_b128 v[208:211], v175 offset:2048
	ds_read_b128 v[214:217], v175 offset:3072
	s_barrier
	s_setprio 1
	s_waitcnt lgkmcnt(0)
	v_mfma_f32_16x16x32_bf16 v[118:121], v[200:203], v[162:165], v[118:121]
	v_lshl_add_u64 v[218:219], v[218:219], 0, s[18:19]
	s_mov_b32 m0, s39
	s_nop 0
	global_load_lds_dwordx4 v[218:219], off
	v_mfma_f32_16x16x32_bf16 v[114:117], v[208:211], v[162:165], v[114:117]
	v_lshl_add_u64 v[218:219], v[220:221], 0, s[18:19]
	s_add_i32 m0, s39, 0x2000
	s_nop 0
	global_load_lds_dwordx4 v[218:219], off
	ds_read_b128 v[162:165], v173 offset:49152
	v_mfma_f32_16x16x32_bf16 v[102:105], v[200:203], v[176:179], v[102:105]
	v_mfma_f32_16x16x32_bf16 v[98:101], v[208:211], v[176:179], v[98:101]
	ds_read_b128 v[176:179], v173 offset:51200
	v_mfma_f32_16x16x32_bf16 v[86:89], v[200:203], v[184:187], v[86:89]
	v_mfma_f32_16x16x32_bf16 v[82:85], v[208:211], v[184:187], v[82:85]
	ds_read_b128 v[184:187], v173 offset:53248
	v_mfma_f32_16x16x32_bf16 v[70:73], v[200:203], v[192:195], v[70:73]
	v_mfma_f32_16x16x32_bf16 v[66:69], v[208:211], v[192:195], v[66:69]
	ds_read_b128 v[192:195], v173 offset:55296
	v_mfma_f32_16x16x32_bf16 v[118:121], v[204:207], v[166:169], v[118:121]
	v_mfma_f32_16x16x32_bf16 v[114:117], v[214:217], v[166:169], v[114:117]
	ds_read_b128 v[166:169], v173 offset:50176
	v_mfma_f32_16x16x32_bf16 v[102:105], v[204:207], v[180:183], v[102:105]
	v_mfma_f32_16x16x32_bf16 v[98:101], v[214:217], v[180:183], v[98:101]
	ds_read_b128 v[180:183], v173 offset:52224
	v_mfma_f32_16x16x32_bf16 v[86:89], v[204:207], v[188:191], v[86:89]
	v_mfma_f32_16x16x32_bf16 v[82:85], v[214:217], v[188:191], v[82:85]
	ds_read_b128 v[188:191], v173 offset:54272
	v_mfma_f32_16x16x32_bf16 v[70:73], v[204:207], v[196:199], v[70:73]
	v_mfma_f32_16x16x32_bf16 v[66:69], v[214:217], v[196:199], v[66:69]
	ds_read_b128 v[196:199], v173 offset:56320
	s_setprio 0
	s_barrier
	s_barrier
	s_setprio 1
	s_waitcnt lgkmcnt(0)
	v_mfma_f32_16x16x32_bf16 v[62:65], v[130:133], v[162:165], v[62:65]
	s_mov_b32 m0, s44
	v_lshl_add_u64 v[218:219], v[222:223], 0, s[18:19]
	s_nop 0
	global_load_lds_dwordx4 v[218:219], off
	v_mfma_f32_16x16x32_bf16 v[58:61], v[138:141], v[162:165], v[58:61]
	v_lshl_add_u64 v[218:219], v[224:225], 0, s[18:19]
	s_mov_b32 m0, s45
	s_nop 0
	global_load_lds_dwordx4 v[218:219], off
	v_mfma_f32_16x16x32_bf16 v[46:49], v[130:133], v[176:179], v[46:49]
	v_mfma_f32_16x16x32_bf16 v[42:45], v[138:141], v[176:179], v[42:45]
	v_mfma_f32_16x16x32_bf16 v[30:33], v[130:133], v[184:187], v[30:33]
	v_mfma_f32_16x16x32_bf16 v[26:29], v[138:141], v[184:187], v[26:29]
	v_mfma_f32_16x16x32_bf16 v[14:17], v[130:133], v[192:195], v[14:17]
	v_mfma_f32_16x16x32_bf16 v[10:13], v[138:141], v[192:195], v[10:13]
	v_mfma_f32_16x16x32_bf16 v[62:65], v[134:137], v[166:169], v[62:65]
	v_mfma_f32_16x16x32_bf16 v[58:61], v[142:145], v[166:169], v[58:61]
	v_mfma_f32_16x16x32_bf16 v[46:49], v[134:137], v[180:183], v[46:49]
	v_mfma_f32_16x16x32_bf16 v[42:45], v[142:145], v[180:183], v[42:45]
	v_mfma_f32_16x16x32_bf16 v[30:33], v[134:137], v[188:191], v[30:33]
	v_mfma_f32_16x16x32_bf16 v[26:29], v[142:145], v[188:191], v[26:29]
	v_mfma_f32_16x16x32_bf16 v[14:17], v[134:137], v[196:199], v[14:17]
	v_mfma_f32_16x16x32_bf16 v[10:13], v[142:145], v[196:199], v[10:13]
	s_setprio 0
	s_barrier
	s_add_u32 s36, s36, 0x80080
	s_addc_u32 s37, s37, 0
	s_add_i32 s38, s38, s5
	v_lshl_add_u64 v[130:131], s[36:37], 0, v[148:149]
	s_mov_b32 m0, s38
	s_nop 0
	global_load_lds_dwordx4 v[130:131], off
	v_lshl_add_u64 v[130:131], s[36:37], 0, v[152:153]
	s_add_i32 m0, s38, 0x2000
	s_nop 0
	global_load_lds_dwordx4 v[130:131], off
	s_waitcnt vmcnt(6)
	s_barrier
	s_setprio 1
	v_mfma_f32_16x16x32_bf16 v[54:57], v[200:203], v[162:165], v[54:57]
	ds_read_b128 v[130:133], v172
	ds_read_b128 v[134:137], v172 offset:1024
	ds_read_b128 v[138:141], v172 offset:2048
	ds_read_b128 v[142:145], v172 offset:3072
	v_mfma_f32_16x16x32_bf16 v[50:53], v[208:211], v[162:165], v[50:53]
	ds_read_b128 v[162:165], v173
	v_mfma_f32_16x16x32_bf16 v[38:41], v[200:203], v[176:179], v[38:41]
	v_mfma_f32_16x16x32_bf16 v[34:37], v[208:211], v[176:179], v[34:37]
	ds_read_b128 v[176:179], v173 offset:2048
	v_mfma_f32_16x16x32_bf16 v[22:25], v[200:203], v[184:187], v[22:25]
	v_mfma_f32_16x16x32_bf16 v[18:21], v[208:211], v[184:187], v[18:21]
	ds_read_b128 v[184:187], v173 offset:4096
	v_mfma_f32_16x16x32_bf16 v[6:9], v[200:203], v[192:195], v[6:9]
	v_mfma_f32_16x16x32_bf16 v[2:5], v[208:211], v[192:195], v[2:5]
	ds_read_b128 v[192:195], v173 offset:6144
	v_mfma_f32_16x16x32_bf16 v[54:57], v[204:207], v[166:169], v[54:57]
	v_mfma_f32_16x16x32_bf16 v[50:53], v[214:217], v[166:169], v[50:53]
	ds_read_b128 v[166:169], v173 offset:1024
	v_mfma_f32_16x16x32_bf16 v[38:41], v[204:207], v[180:183], v[38:41]
	v_mfma_f32_16x16x32_bf16 v[34:37], v[214:217], v[180:183], v[34:37]
	ds_read_b128 v[180:183], v173 offset:3072
	v_mfma_f32_16x16x32_bf16 v[22:25], v[204:207], v[188:191], v[22:25]
	v_mfma_f32_16x16x32_bf16 v[18:21], v[214:217], v[188:191], v[18:21]
	ds_read_b128 v[188:191], v173 offset:5120
	v_mfma_f32_16x16x32_bf16 v[6:9], v[204:207], v[196:199], v[6:9]
	v_mfma_f32_16x16x32_bf16 v[2:5], v[214:217], v[196:199], v[2:5]
	ds_read_b128 v[196:199], v173 offset:7168
	s_setprio 0
	s_add_u32 s8, s8, 0x100
	s_addc_u32 s9, s9, 0
	s_add_u32 s53, s53, 0x100
	s_addc_u32 s54, s54, 0
	s_cmp_ge_i32 s55, s1
	s_mov_b32 s36, s55
	s_barrier
	s_cbranch_scc0 .LBB0_964
	s_branch .Lmy_pl1_exit
.LBB0_964:
	s_add_i32 s55, s36, 2
	s_add_u32 s37, s8, 0xfff80080
	s_addc_u32 s38, s9, -1
	s_cmp_eq_u32 s46, s36
	s_cselect_b32 s36, s52, s53
	s_cselect_b32 s39, s25, s38
	s_cselect_b32 s38, s27, s37
	s_cselect_b32 s37, s51, s54
	v_lshl_add_u64 v[200:201], s[8:9], 0, v[154:155]
	s_add_i32 m0, s23, 0xc000
	global_load_lds_dwordx4 v[200:201], off
	v_lshl_add_u64 v[200:201], s[8:9], 0, v[156:157]
	s_add_i32 m0, s23, 0xe000
	s_nop 0
	global_load_lds_dwordx4 v[200:201], off
	s_waitcnt lgkmcnt(8)
	s_barrier
	s_setprio 1
	s_waitcnt lgkmcnt(0)
	v_mfma_f32_16x16x32_bf16 v[126:129], v[130:133], v[162:165], v[126:129]
	ds_read_b128 v[200:203], v174
	ds_read_b128 v[204:207], v174 offset:1024
	ds_read_b128 v[208:211], v174 offset:2048
	ds_read_b128 v[214:217], v174 offset:3072
	v_mfma_f32_16x16x32_bf16 v[122:125], v[138:141], v[162:165], v[122:125]
	v_mfma_f32_16x16x32_bf16 v[110:113], v[130:133], v[176:179], v[110:113]
	v_mfma_f32_16x16x32_bf16 v[106:109], v[138:141], v[176:179], v[106:109]
	v_mfma_f32_16x16x32_bf16 v[94:97], v[130:133], v[184:187], v[94:97]
	v_mfma_f32_16x16x32_bf16 v[90:93], v[138:141], v[184:187], v[90:93]
	v_mfma_f32_16x16x32_bf16 v[78:81], v[130:133], v[192:195], v[78:81]
	v_mfma_f32_16x16x32_bf16 v[74:77], v[138:141], v[192:195], v[74:77]
	v_mfma_f32_16x16x32_bf16 v[126:129], v[134:137], v[166:169], v[126:129]
	v_mfma_f32_16x16x32_bf16 v[122:125], v[142:145], v[166:169], v[122:125]
	v_mfma_f32_16x16x32_bf16 v[110:113], v[134:137], v[180:183], v[110:113]
	v_mfma_f32_16x16x32_bf16 v[106:109], v[142:145], v[180:183], v[106:109]
	v_mfma_f32_16x16x32_bf16 v[94:97], v[134:137], v[188:191], v[94:97]
	v_mfma_f32_16x16x32_bf16 v[90:93], v[142:145], v[188:191], v[90:93]
	v_mfma_f32_16x16x32_bf16 v[78:81], v[134:137], v[196:199], v[78:81]
	v_mfma_f32_16x16x32_bf16 v[74:77], v[142:145], v[196:199], v[74:77]
	s_setprio 0
	s_barrier
	s_add_i32 s56, s48, s5
	s_barrier
	s_setprio 1
	s_waitcnt lgkmcnt(0)
	v_mfma_f32_16x16x32_bf16 v[118:121], v[200:203], v[162:165], v[118:121]
	v_lshl_add_u64 v[218:219], s[36:37], 0, v[148:149]
	s_mov_b32 m0, s56
	s_nop 0
	global_load_lds_dwordx4 v[218:219], off
	v_mfma_f32_16x16x32_bf16 v[114:117], v[208:211], v[162:165], v[114:117]
	v_lshl_add_u64 v[220:221], s[36:37], 0, v[152:153]
	s_add_i32 m0, s56, 0x2000
	s_nop 0
	global_load_lds_dwordx4 v[220:221], off
	ds_read_b128 v[162:165], v173 offset:16384
	v_mfma_f32_16x16x32_bf16 v[102:105], v[200:203], v[176:179], v[102:105]
	v_mfma_f32_16x16x32_bf16 v[98:101], v[208:211], v[176:179], v[98:101]
	ds_read_b128 v[176:179], v173 offset:18432
	v_mfma_f32_16x16x32_bf16 v[86:89], v[200:203], v[184:187], v[86:89]
	v_mfma_f32_16x16x32_bf16 v[82:85], v[208:211], v[184:187], v[82:85]
	ds_read_b128 v[184:187], v173 offset:20480
	v_mfma_f32_16x16x32_bf16 v[70:73], v[200:203], v[192:195], v[70:73]
	v_mfma_f32_16x16x32_bf16 v[66:69], v[208:211], v[192:195], v[66:69]
	ds_read_b128 v[192:195], v173 offset:22528
	v_mfma_f32_16x16x32_bf16 v[118:121], v[204:207], v[166:169], v[118:121]
	v_mfma_f32_16x16x32_bf16 v[114:117], v[214:217], v[166:169], v[114:117]
	ds_read_b128 v[166:169], v173 offset:17408
	v_mfma_f32_16x16x32_bf16 v[102:105], v[204:207], v[180:183], v[102:105]
	v_mfma_f32_16x16x32_bf16 v[98:101], v[214:217], v[180:183], v[98:101]
	ds_read_b128 v[180:183], v173 offset:19456
	v_mfma_f32_16x16x32_bf16 v[86:89], v[204:207], v[188:191], v[86:89]
	v_mfma_f32_16x16x32_bf16 v[82:85], v[214:217], v[188:191], v[82:85]
	ds_read_b128 v[188:191], v173 offset:21504
	v_mfma_f32_16x16x32_bf16 v[70:73], v[204:207], v[196:199], v[70:73]
	v_mfma_f32_16x16x32_bf16 v[66:69], v[214:217], v[196:199], v[66:69]
	ds_read_b128 v[196:199], v173 offset:23552
	s_setprio 0
	s_barrier
	s_barrier
	s_setprio 1
	s_waitcnt lgkmcnt(0)
	v_mfma_f32_16x16x32_bf16 v[62:65], v[130:133], v[162:165], v[62:65]
	s_mov_b32 m0, s23
	v_lshl_add_u64 v[222:223], s[38:39], 0, v[146:147]
	s_nop 0
	global_load_lds_dwordx4 v[222:223], off
	v_mfma_f32_16x16x32_bf16 v[58:61], v[138:141], v[162:165], v[58:61]
	v_lshl_add_u64 v[224:225], s[38:39], 0, v[150:151]
	s_mov_b32 m0, s33
	s_nop 0
	global_load_lds_dwordx4 v[224:225], off
	v_mfma_f32_16x16x32_bf16 v[46:49], v[130:133], v[176:179], v[46:49]
	v_mfma_f32_16x16x32_bf16 v[42:45], v[138:141], v[176:179], v[42:45]
	v_mfma_f32_16x16x32_bf16 v[30:33], v[130:133], v[184:187], v[30:33]
	v_mfma_f32_16x16x32_bf16 v[26:29], v[138:141], v[184:187], v[26:29]
	v_mfma_f32_16x16x32_bf16 v[14:17], v[130:133], v[192:195], v[14:17]
	v_mfma_f32_16x16x32_bf16 v[10:13], v[138:141], v[192:195], v[10:13]
	v_mfma_f32_16x16x32_bf16 v[62:65], v[134:137], v[166:169], v[62:65]
	v_mfma_f32_16x16x32_bf16 v[58:61], v[142:145], v[166:169], v[58:61]
	v_mfma_f32_16x16x32_bf16 v[46:49], v[134:137], v[180:183], v[46:49]
	v_mfma_f32_16x16x32_bf16 v[42:45], v[142:145], v[180:183], v[42:45]
	v_mfma_f32_16x16x32_bf16 v[30:33], v[134:137], v[188:191], v[30:33]
	v_mfma_f32_16x16x32_bf16 v[26:29], v[142:145], v[188:191], v[26:29]
	v_mfma_f32_16x16x32_bf16 v[14:17], v[134:137], v[196:199], v[14:17]
	v_mfma_f32_16x16x32_bf16 v[10:13], v[142:145], v[196:199], v[10:13]
	s_setprio 0
	s_barrier
	s_add_u32 s56, s36, 0x80000
	s_addc_u32 s57, s37, 0
	s_add_i32 s58, s49, s5
	v_lshl_add_u64 v[130:131], s[56:57], 0, v[148:149]
	s_mov_b32 m0, s58
	s_nop 0
	global_load_lds_dwordx4 v[130:131], off
	v_lshl_add_u64 v[130:131], s[56:57], 0, v[152:153]
	s_add_i32 m0, s58, 0x2000
	s_nop 0
	global_load_lds_dwordx4 v[130:131], off
	s_waitcnt vmcnt(6)
	s_barrier
	s_setprio 1
	v_mfma_f32_16x16x32_bf16 v[54:57], v[200:203], v[162:165], v[54:57]
	v_mfma_f32_16x16x32_bf16 v[50:53], v[208:211], v[162:165], v[50:53]
	ds_read_b128 v[162:165], v173 offset:32768
	v_mfma_f32_16x16x32_bf16 v[38:41], v[200:203], v[176:179], v[38:41]
	v_mfma_f32_16x16x32_bf16 v[34:37], v[208:211], v[176:179], v[34:37]
	ds_read_b128 v[176:179], v173 offset:34816
	v_mfma_f32_16x16x32_bf16 v[22:25], v[200:203], v[184:187], v[22:25]
	v_mfma_f32_16x16x32_bf16 v[18:21], v[208:211], v[184:187], v[18:21]
	ds_read_b128 v[184:187], v173 offset:36864
	v_mfma_f32_16x16x32_bf16 v[6:9], v[200:203], v[192:195], v[6:9]
	v_mfma_f32_16x16x32_bf16 v[2:5], v[208:211], v[192:195], v[2:5]
	ds_read_b128 v[192:195], v173 offset:38912
	v_mfma_f32_16x16x32_bf16 v[54:57], v[204:207], v[166:169], v[54:57]
	v_mfma_f32_16x16x32_bf16 v[50:53], v[214:217], v[166:169], v[50:53]
	ds_read_b128 v[166:169], v173 offset:33792
	v_mfma_f32_16x16x32_bf16 v[38:41], v[204:207], v[180:183], v[38:41]
	v_mfma_f32_16x16x32_bf16 v[34:37], v[214:217], v[180:183], v[34:37]
	ds_read_b128 v[180:183], v173 offset:35840
	v_mfma_f32_16x16x32_bf16 v[22:25], v[204:207], v[188:191], v[22:25]
	v_mfma_f32_16x16x32_bf16 v[18:21], v[214:217], v[188:191], v[18:21]
	ds_read_b128 v[188:191], v173 offset:37888
	v_mfma_f32_16x16x32_bf16 v[6:9], v[204:207], v[196:199], v[6:9]
	v_mfma_f32_16x16x32_bf16 v[2:5], v[214:217], v[196:199], v[2:5]
	ds_read_b128 v[196:199], v173 offset:39936
	s_setprio 0
	s_add_i32 s56, 0, 0x18000
	v_add_u32_e32 v142, s56, v171
	s_barrier
	ds_read_b128 v[130:133], v142
	ds_read_b128 v[134:137], v142 offset:1024
	ds_read_b128 v[138:141], v142 offset:2048
	ds_read_b128 v[142:145], v142 offset:3072
	s_add_u32 s38, s38, 0x80000
	s_addc_u32 s39, s39, 0
	s_waitcnt lgkmcnt(8)
	s_barrier
	s_setprio 1
	s_waitcnt lgkmcnt(0)
	v_mfma_f32_16x16x32_bf16 v[126:129], v[130:133], v[162:165], v[126:129]
	s_mov_b32 m0, s35
	v_lshl_add_u64 v[200:201], s[38:39], 0, v[146:147]
	s_nop 0
	global_load_lds_dwordx4 v[200:201], off
	v_mfma_f32_16x16x32_bf16 v[122:125], v[138:141], v[162:165], v[122:125]
	v_lshl_add_u64 v[200:201], s[38:39], 0, v[150:151]
	s_mov_b32 m0, s40
	s_nop 0
	global_load_lds_dwordx4 v[200:201], off
	v_mfma_f32_16x16x32_bf16 v[110:113], v[130:133], v[176:179], v[110:113]
	v_mfma_f32_16x16x32_bf16 v[106:109], v[138:141], v[176:179], v[106:109]
	v_mfma_f32_16x16x32_bf16 v[94:97], v[130:133], v[184:187], v[94:97]
	v_mfma_f32_16x16x32_bf16 v[90:93], v[138:141], v[184:187], v[90:93]
	v_mfma_f32_16x16x32_bf16 v[78:81], v[130:133], v[192:195], v[78:81]
	v_mfma_f32_16x16x32_bf16 v[74:77], v[138:141], v[192:195], v[74:77]
	v_mfma_f32_16x16x32_bf16 v[126:129], v[134:137], v[166:169], v[126:129]
	v_mfma_f32_16x16x32_bf16 v[122:125], v[142:145], v[166:169], v[122:125]
	v_mfma_f32_16x16x32_bf16 v[110:113], v[134:137], v[180:183], v[110:113]
	v_mfma_f32_16x16x32_bf16 v[106:109], v[142:145], v[180:183], v[106:109]
	v_mfma_f32_16x16x32_bf16 v[94:97], v[134:137], v[188:191], v[94:97]
	v_mfma_f32_16x16x32_bf16 v[90:93], v[142:145], v[188:191], v[90:93]
	v_mfma_f32_16x16x32_bf16 v[78:81], v[134:137], v[196:199], v[78:81]
	v_mfma_f32_16x16x32_bf16 v[74:77], v[142:145], v[196:199], v[74:77]
	s_setprio 0
	s_barrier
	s_add_i32 s38, 0, 0x1c000
	s_add_i32 s39, s56, s5
	v_add_u32_e32 v175, s38, v171
	ds_read_b128 v[200:203], v175
	ds_read_b128 v[204:207], v175 offset:1024
	ds_read_b128 v[208:211], v175 offset:2048
	ds_read_b128 v[214:217], v175 offset:3072
	s_barrier
	s_setprio 1
	s_waitcnt lgkmcnt(0)
	v_mfma_f32_16x16x32_bf16 v[118:121], v[200:203], v[162:165], v[118:121]
	v_lshl_add_u64 v[218:219], v[218:219], 0, s[18:19]
	s_mov_b32 m0, s39
	s_nop 0
	global_load_lds_dwordx4 v[218:219], off
	v_mfma_f32_16x16x32_bf16 v[114:117], v[208:211], v[162:165], v[114:117]
	v_lshl_add_u64 v[218:219], v[220:221], 0, s[18:19]
	s_add_i32 m0, s39, 0x2000
	s_nop 0
	global_load_lds_dwordx4 v[218:219], off
	ds_read_b128 v[162:165], v173 offset:49152
	v_mfma_f32_16x16x32_bf16 v[102:105], v[200:203], v[176:179], v[102:105]
	v_mfma_f32_16x16x32_bf16 v[98:101], v[208:211], v[176:179], v[98:101]
	ds_read_b128 v[176:179], v173 offset:51200
	v_mfma_f32_16x16x32_bf16 v[86:89], v[200:203], v[184:187], v[86:89]
	v_mfma_f32_16x16x32_bf16 v[82:85], v[208:211], v[184:187], v[82:85]
	ds_read_b128 v[184:187], v173 offset:53248
	v_mfma_f32_16x16x32_bf16 v[70:73], v[200:203], v[192:195], v[70:73]
	v_mfma_f32_16x16x32_bf16 v[66:69], v[208:211], v[192:195], v[66:69]
	ds_read_b128 v[192:195], v173 offset:55296
	v_mfma_f32_16x16x32_bf16 v[118:121], v[204:207], v[166:169], v[118:121]
	v_mfma_f32_16x16x32_bf16 v[114:117], v[214:217], v[166:169], v[114:117]
	ds_read_b128 v[166:169], v173 offset:50176
	v_mfma_f32_16x16x32_bf16 v[102:105], v[204:207], v[180:183], v[102:105]
	v_mfma_f32_16x16x32_bf16 v[98:101], v[214:217], v[180:183], v[98:101]
	ds_read_b128 v[180:183], v173 offset:52224
	v_mfma_f32_16x16x32_bf16 v[86:89], v[204:207], v[188:191], v[86:89]
	v_mfma_f32_16x16x32_bf16 v[82:85], v[214:217], v[188:191], v[82:85]
	ds_read_b128 v[188:191], v173 offset:54272
	v_mfma_f32_16x16x32_bf16 v[70:73], v[204:207], v[196:199], v[70:73]
	v_mfma_f32_16x16x32_bf16 v[66:69], v[214:217], v[196:199], v[66:69]
	ds_read_b128 v[196:199], v173 offset:56320
	s_setprio 0
	s_barrier
	s_barrier
	s_setprio 1
	s_waitcnt lgkmcnt(0)
	v_mfma_f32_16x16x32_bf16 v[62:65], v[130:133], v[162:165], v[62:65]
	s_mov_b32 m0, s44
	v_lshl_add_u64 v[218:219], v[222:223], 0, s[18:19]
	s_nop 0
	global_load_lds_dwordx4 v[218:219], off
	v_mfma_f32_16x16x32_bf16 v[58:61], v[138:141], v[162:165], v[58:61]
	v_lshl_add_u64 v[218:219], v[224:225], 0, s[18:19]
	s_mov_b32 m0, s45
	s_nop 0
	global_load_lds_dwordx4 v[218:219], off
	v_mfma_f32_16x16x32_bf16 v[46:49], v[130:133], v[176:179], v[46:49]
	v_mfma_f32_16x16x32_bf16 v[42:45], v[138:141], v[176:179], v[42:45]
	v_mfma_f32_16x16x32_bf16 v[30:33], v[130:133], v[184:187], v[30:33]
	v_mfma_f32_16x16x32_bf16 v[26:29], v[138:141], v[184:187], v[26:29]
	v_mfma_f32_16x16x32_bf16 v[14:17], v[130:133], v[192:195], v[14:17]
	v_mfma_f32_16x16x32_bf16 v[10:13], v[138:141], v[192:195], v[10:13]
	v_mfma_f32_16x16x32_bf16 v[62:65], v[134:137], v[166:169], v[62:65]
	v_mfma_f32_16x16x32_bf16 v[58:61], v[142:145], v[166:169], v[58:61]
	v_mfma_f32_16x16x32_bf16 v[46:49], v[134:137], v[180:183], v[46:49]
	v_mfma_f32_16x16x32_bf16 v[42:45], v[142:145], v[180:183], v[42:45]
	v_mfma_f32_16x16x32_bf16 v[30:33], v[134:137], v[188:191], v[30:33]
	v_mfma_f32_16x16x32_bf16 v[26:29], v[142:145], v[188:191], v[26:29]
	v_mfma_f32_16x16x32_bf16 v[14:17], v[134:137], v[196:199], v[14:17]
	v_mfma_f32_16x16x32_bf16 v[10:13], v[142:145], v[196:199], v[10:13]
	s_setprio 0
	s_barrier
	s_add_u32 s36, s36, 0x80080
	s_addc_u32 s37, s37, 0
	s_add_i32 s38, s38, s5
	v_lshl_add_u64 v[130:131], s[36:37], 0, v[148:149]
	s_mov_b32 m0, s38
	s_nop 0
	global_load_lds_dwordx4 v[130:131], off
	v_lshl_add_u64 v[130:131], s[36:37], 0, v[152:153]
	s_add_i32 m0, s38, 0x2000
	s_nop 0
	global_load_lds_dwordx4 v[130:131], off
	s_waitcnt vmcnt(6)
	s_barrier
	s_setprio 1
	v_mfma_f32_16x16x32_bf16 v[54:57], v[200:203], v[162:165], v[54:57]
	ds_read_b128 v[130:133], v172
	ds_read_b128 v[134:137], v172 offset:1024
	ds_read_b128 v[138:141], v172 offset:2048
	ds_read_b128 v[142:145], v172 offset:3072
	v_mfma_f32_16x16x32_bf16 v[50:53], v[208:211], v[162:165], v[50:53]
	ds_read_b128 v[162:165], v173
	v_mfma_f32_16x16x32_bf16 v[38:41], v[200:203], v[176:179], v[38:41]
	v_mfma_f32_16x16x32_bf16 v[34:37], v[208:211], v[176:179], v[34:37]
	ds_read_b128 v[176:179], v173 offset:2048
	v_mfma_f32_16x16x32_bf16 v[22:25], v[200:203], v[184:187], v[22:25]
	v_mfma_f32_16x16x32_bf16 v[18:21], v[208:211], v[184:187], v[18:21]
	ds_read_b128 v[184:187], v173 offset:4096
	v_mfma_f32_16x16x32_bf16 v[6:9], v[200:203], v[192:195], v[6:9]
	v_mfma_f32_16x16x32_bf16 v[2:5], v[208:211], v[192:195], v[2:5]
	ds_read_b128 v[192:195], v173 offset:6144
	v_mfma_f32_16x16x32_bf16 v[54:57], v[204:207], v[166:169], v[54:57]
	v_mfma_f32_16x16x32_bf16 v[50:53], v[214:217], v[166:169], v[50:53]
	ds_read_b128 v[166:169], v173 offset:1024
	v_mfma_f32_16x16x32_bf16 v[38:41], v[204:207], v[180:183], v[38:41]
	v_mfma_f32_16x16x32_bf16 v[34:37], v[214:217], v[180:183], v[34:37]
	ds_read_b128 v[180:183], v173 offset:3072
	v_mfma_f32_16x16x32_bf16 v[22:25], v[204:207], v[188:191], v[22:25]
	v_mfma_f32_16x16x32_bf16 v[18:21], v[214:217], v[188:191], v[18:21]
	ds_read_b128 v[188:191], v173 offset:5120
	v_mfma_f32_16x16x32_bf16 v[6:9], v[204:207], v[196:199], v[6:9]
	v_mfma_f32_16x16x32_bf16 v[2:5], v[214:217], v[196:199], v[2:5]
	ds_read_b128 v[196:199], v173 offset:7168
	s_setprio 0
	s_add_u32 s8, s8, 0x100
	s_addc_u32 s9, s9, 0
	s_add_u32 s53, s53, 0x100
	s_addc_u32 s54, s54, 0
	s_cmp_ge_i32 s55, s1
	s_mov_b32 s36, s55
	s_barrier
	s_cbranch_scc0 .LBB0_964

.Lmy_pl2_1553:
	s_add_i32 s71, s71, 2
	s_add_u32 s30, s28, 0x100
	s_addc_u32 s31, s29, 0
	s_and_b64 s[36:37], s[34:35], exec
	s_cselect_b32 s36, 0, s30
	s_cselect_b32 s37, 0, s31
	s_add_u32 s36, s22, s36
	s_addc_u32 s37, s23, s37
	s_add_u32 s72, s69, s28
	s_addc_u32 s73, s70, s29
	s_and_b64 s[28:29], s[34:35], exec
	s_cselect_b32 s29, s67, s73
	s_cselect_b32 s28, s68, s72
	s_mov_b32 m0, s42
	v_add_u32_e32 v191, s57, v204
	v_lshl_add_u64 v[230:231], s[28:29], 0, v[188:189]
	v_add_u32_e32 v197, s57, v205
	ds_read_b128 v[214:217], v191
	ds_read_b128 v[222:225], v191 offset:2048
	ds_read_b128 v[218:221], v197
	ds_read_b128 v[226:229], v197 offset:2048
	global_load_lds_dwordx4 v[230:231], off
	v_lshl_add_u64 v[232:233], s[28:29], 0, v[186:187]
	s_mov_b32 m0, s43
	v_mfma_scale_f32_16x16x128_f8f6f4 v[174:177], v[2:9], v[26:33], 0, v211, v210 op_sel_hi:[0,0,0]
	global_load_lds_dwordx4 v[232:233], off
	s_barrier
	v_mov_b32_e32 v193, v185
	v_mov_b32_e32 v195, v185
	v_mfma_scale_f32_16x16x128_f8f6f4 v[170:173], v[10:17], v[26:33], 0, v211, v210 op_sel_hi:[0,0,0]
	v_mfma_scale_f32_16x16x128_f8f6f4 v[166:169], v[2:9], v[18:25], 0, v211, v210 op_sel_hi:[0,0,0]
	v_mfma_scale_f32_16x16x128_f8f6f4 v[162:165], v[10:17], v[18:25], 0, v211, v210 op_sel_hi:[0,0,0]
	v_mfma_scale_f32_16x16x128_f8f6f4 v[142:145], v[2:9], v[42:49], 0, v211, v210 op_sel_hi:[0,0,0]
	v_mfma_scale_f32_16x16x128_f8f6f4 v[130:133], v[10:17], v[42:49], 0, v211, v210 op_sel_hi:[0,0,0]
	v_mfma_scale_f32_16x16x128_f8f6f4 v[118:121], v[2:9], v[34:41], 0, v211, v210 op_sel_hi:[0,0,0]
	v_mfma_scale_f32_16x16x128_f8f6f4 v[114:117], v[10:17], v[34:41], 0, v211, v210 op_sel_hi:[0,0,0]
	s_setprio 1
	s_waitcnt lgkmcnt(0)
	v_mfma_scale_f32_16x16x128_f8f6f4 v[158:161], v[214:221], v[26:33], 0, v211, v210 op_sel_hi:[0,0,0]
	v_mfma_scale_f32_16x16x128_f8f6f4 v[154:157], v[222:229], v[26:33], 0, v211, v210 op_sel_hi:[0,0,0]
	ds_read_b128 v[26:29], v208 offset:18432
	ds_read_b128 v[30:33], v209 offset:18432
	v_mfma_scale_f32_16x16x128_f8f6f4 v[150:153], v[214:221], v[18:25], 0, v211, v210 op_sel_hi:[0,0,0]
	v_mfma_scale_f32_16x16x128_f8f6f4 v[146:149], v[222:229], v[18:25], 0, v211, v210 op_sel_hi:[0,0,0]
	ds_read_b128 v[18:21], v208 offset:16384
	ds_read_b128 v[22:25], v209 offset:16384
	v_mfma_scale_f32_16x16x128_f8f6f4 v[138:141], v[214:221], v[42:49], 0, v211, v210 op_sel_hi:[0,0,0]
	v_mfma_scale_f32_16x16x128_f8f6f4 v[134:137], v[222:229], v[42:49], 0, v211, v210 op_sel_hi:[0,0,0]
	ds_read_b128 v[42:45], v208 offset:22528
	ds_read_b128 v[46:49], v209 offset:22528
	v_mfma_scale_f32_16x16x128_f8f6f4 v[126:129], v[214:221], v[34:41], 0, v211, v210 op_sel_hi:[0,0,0]
	v_mfma_scale_f32_16x16x128_f8f6f4 v[122:125], v[222:229], v[34:41], 0, v211, v210 op_sel_hi:[0,0,0]
	ds_read_b128 v[34:37], v208 offset:20480
	ds_read_b128 v[38:41], v209 offset:20480
	s_setprio 0
	s_barrier
	v_mov_b32_e32 v191, v185
	s_barrier
	v_lshl_add_u64 v[234:235], s[36:37], 0, v[184:185]
	v_lshl_add_u64 v[236:237], s[36:37], 0, v[190:191]
	s_setprio 1
	s_waitcnt lgkmcnt(0)
	v_mfma_scale_f32_16x16x128_f8f6f4 v[110:113], v[2:9], v[18:25], 0, v211, v210 op_sel_hi:[0,0,0]
	s_mov_b32 m0, s41
	s_nop 0
	global_load_lds_dwordx4 v184, s[36:37]
	v_mfma_scale_f32_16x16x128_f8f6f4 v[102:105], v[10:17], v[18:25], 0, v211, v210 op_sel_hi:[0,0,0]
	s_mov_b32 m0, s44
	s_nop 0
	global_load_lds_dwordx4 v190, s[36:37]
	v_mfma_scale_f32_16x16x128_f8f6f4 v[94:97], v[2:9], v[26:33], 0, v211, v210 op_sel_hi:[0,0,0]
	v_mfma_scale_f32_16x16x128_f8f6f4 v[86:89], v[10:17], v[26:33], 0, v211, v210 op_sel_hi:[0,0,0]
	v_mfma_scale_f32_16x16x128_f8f6f4 v[78:81], v[2:9], v[34:41], 0, v211, v210 op_sel_hi:[0,0,0]
	v_mfma_scale_f32_16x16x128_f8f6f4 v[70:73], v[10:17], v[34:41], 0, v211, v210 op_sel_hi:[0,0,0]
	v_mfma_scale_f32_16x16x128_f8f6f4 v[62:65], v[2:9], v[42:49], 0, v211, v210 op_sel_hi:[0,0,0]
	v_mfma_scale_f32_16x16x128_f8f6f4 v[54:57], v[10:17], v[42:49], 0, v211, v210 op_sel_hi:[0,0,0]
	s_setprio 0
	s_barrier
	s_add_u32 s34, s28, 0x40000
	s_addc_u32 s35, s29, 0
	s_mov_b32 m0, s59
	v_lshl_add_u64 v[2:3], s[34:35], 0, v[188:189]
	global_load_lds_dwordx4 v[2:3], off
	v_lshl_add_u64 v[2:3], s[34:35], 0, v[186:187]
	s_mov_b32 m0, s60
	s_nop 0
	global_load_lds_dwordx4 v[2:3], off
	s_waitcnt vmcnt(6)
	s_barrier
	s_setprio 1
	v_mfma_scale_f32_16x16x128_f8f6f4 v[106:109], v[214:221], v[18:25], 0, v211, v210 op_sel_hi:[0,0,0]
	v_mfma_scale_f32_16x16x128_f8f6f4 v[98:101], v[222:229], v[18:25], 0, v211, v210 op_sel_hi:[0,0,0]
	ds_read_b128 v[18:21], v208 offset:32768
	ds_read_b128 v[22:25], v209 offset:32768
	v_mfma_scale_f32_16x16x128_f8f6f4 v[90:93], v[214:221], v[26:33], 0, v211, v210 op_sel_hi:[0,0,0]
	v_mfma_scale_f32_16x16x128_f8f6f4 v[82:85], v[222:229], v[26:33], 0, v211, v210 op_sel_hi:[0,0,0]
	ds_read_b128 v[26:29], v208 offset:34816
	ds_read_b128 v[30:33], v209 offset:34816
	v_mfma_scale_f32_16x16x128_f8f6f4 v[74:77], v[214:221], v[34:41], 0, v211, v210 op_sel_hi:[0,0,0]
	v_mfma_scale_f32_16x16x128_f8f6f4 v[66:69], v[222:229], v[34:41], 0, v211, v210 op_sel_hi:[0,0,0]
	ds_read_b128 v[34:37], v208 offset:36864
	ds_read_b128 v[38:41], v209 offset:36864
	v_mfma_scale_f32_16x16x128_f8f6f4 v[58:61], v[214:221], v[42:49], 0, v211, v210 op_sel_hi:[0,0,0]
	v_mfma_scale_f32_16x16x128_f8f6f4 v[50:53], v[222:229], v[42:49], 0, v211, v210 op_sel_hi:[0,0,0]
	ds_read_b128 v[42:45], v208 offset:38912
	ds_read_b128 v[46:49], v209 offset:38912
	s_setprio 0
	v_add_u32_e32 v6, s61, v204
	v_add_u32_e32 v14, s61, v205
	s_barrier
	ds_read_b128 v[2:5], v6
	ds_read_b128 v[10:13], v6 offset:2048
	ds_read_b128 v[6:9], v14
	ds_read_b128 v[14:17], v14 offset:2048
	s_waitcnt lgkmcnt(8)
	s_barrier
	s_setprio 1
	s_waitcnt lgkmcnt(0)
	v_mfma_scale_f32_16x16x128_f8f6f4 v[174:177], v[2:9], v[18:25], v[174:177], v211, v210 op_sel_hi:[0,0,0]
	s_mov_b32 m0, s45
	v_lshl_add_u64 v[214:215], s[36:37], 0, v[192:193]
	s_nop 0
	global_load_lds_dwordx4 v[214:215], off
	v_mfma_scale_f32_16x16x128_f8f6f4 v[170:173], v[10:17], v[18:25], v[170:173], v211, v210 op_sel_hi:[0,0,0]
	v_lshl_add_u64 v[214:215], s[36:37], 0, v[194:195]
	s_mov_b32 m0, s46
	s_nop 0
	global_load_lds_dwordx4 v[214:215], off
	v_mfma_scale_f32_16x16x128_f8f6f4 v[166:169], v[2:9], v[26:33], v[166:169], v211, v210 op_sel_hi:[0,0,0]
	v_mfma_scale_f32_16x16x128_f8f6f4 v[162:165], v[10:17], v[26:33], v[162:165], v211, v210 op_sel_hi:[0,0,0]
	v_mfma_scale_f32_16x16x128_f8f6f4 v[142:145], v[2:9], v[34:41], v[142:145], v211, v210 op_sel_hi:[0,0,0]
	v_mfma_scale_f32_16x16x128_f8f6f4 v[130:133], v[10:17], v[34:41], v[130:133], v211, v210 op_sel_hi:[0,0,0]
	v_mfma_scale_f32_16x16x128_f8f6f4 v[118:121], v[2:9], v[42:49], v[118:121], v211, v210 op_sel_hi:[0,0,0]
	v_mfma_scale_f32_16x16x128_f8f6f4 v[114:117], v[10:17], v[42:49], v[114:117], v211, v210 op_sel_hi:[0,0,0]
	s_setprio 0
	s_barrier
	v_add_u32_e32 v191, s62, v204
	v_add_u32_e32 v193, s62, v205
	ds_read_b128 v[214:217], v191
	ds_read_b128 v[222:225], v191 offset:2048
	ds_read_b128 v[218:221], v193
	ds_read_b128 v[226:229], v193 offset:2048
	s_barrier
	s_setprio 1
	s_waitcnt lgkmcnt(0)
	v_mfma_scale_f32_16x16x128_f8f6f4 v[158:161], v[214:221], v[18:25], v[158:161], v211, v210 op_sel_hi:[0,0,0]
	s_mov_b32 m0, s63
	v_lshl_add_u64 v[230:231], v[230:231], 0, s[12:13]
	s_nop 0
	global_load_lds_dwordx4 v[230:231], off
	v_mfma_scale_f32_16x16x128_f8f6f4 v[154:157], v[222:229], v[18:25], v[154:157], v211, v210 op_sel_hi:[0,0,0]
	v_lshl_add_u64 v[230:231], v[232:233], 0, s[12:13]
	s_add_i32 m0, s63, 0x2000
	s_nop 0
	global_load_lds_dwordx4 v[230:231], off
	ds_read_b128 v[18:21], v208 offset:49152
	ds_read_b128 v[22:25], v209 offset:49152
	v_mfma_scale_f32_16x16x128_f8f6f4 v[150:153], v[214:221], v[26:33], v[150:153], v211, v210 op_sel_hi:[0,0,0]
	v_mfma_scale_f32_16x16x128_f8f6f4 v[146:149], v[222:229], v[26:33], v[146:149], v211, v210 op_sel_hi:[0,0,0]
	ds_read_b128 v[26:29], v208 offset:51200
	ds_read_b128 v[30:33], v209 offset:51200
	v_mfma_scale_f32_16x16x128_f8f6f4 v[138:141], v[214:221], v[34:41], v[138:141], v211, v210 op_sel_hi:[0,0,0]
	v_mfma_scale_f32_16x16x128_f8f6f4 v[134:137], v[222:229], v[34:41], v[134:137], v211, v210 op_sel_hi:[0,0,0]
	ds_read_b128 v[34:37], v208 offset:53248
	ds_read_b128 v[38:41], v209 offset:53248
	v_mfma_scale_f32_16x16x128_f8f6f4 v[126:129], v[214:221], v[42:49], v[126:129], v211, v210 op_sel_hi:[0,0,0]
	v_mfma_scale_f32_16x16x128_f8f6f4 v[122:125], v[222:229], v[42:49], v[122:125], v211, v210 op_sel_hi:[0,0,0]
	ds_read_b128 v[42:45], v208 offset:55296
	ds_read_b128 v[46:49], v209 offset:55296
	s_setprio 0
	s_barrier
	s_barrier
	s_setprio 1
	s_waitcnt lgkmcnt(0)
	v_mfma_scale_f32_16x16x128_f8f6f4 v[110:113], v[2:9], v[18:25], v[110:113], v211, v210 op_sel_hi:[0,0,0]
	s_mov_b32 m0, s49
	v_lshl_add_u64 v[230:231], v[234:235], 0, s[12:13]
	s_nop 0
	global_load_lds_dwordx4 v[230:231], off
	v_mfma_scale_f32_16x16x128_f8f6f4 v[102:105], v[10:17], v[18:25], v[102:105], v211, v210 op_sel_hi:[0,0,0]
	v_lshl_add_u64 v[230:231], v[236:237], 0, s[12:13]
	s_mov_b32 m0, s50
	s_nop 0
	global_load_lds_dwordx4 v[230:231], off
	v_mfma_scale_f32_16x16x128_f8f6f4 v[94:97], v[2:9], v[26:33], v[94:97], v211, v210 op_sel_hi:[0,0,0]
	v_mfma_scale_f32_16x16x128_f8f6f4 v[86:89], v[10:17], v[26:33], v[86:89], v211, v210 op_sel_hi:[0,0,0]
	v_mfma_scale_f32_16x16x128_f8f6f4 v[78:81], v[2:9], v[34:41], v[78:81], v211, v210 op_sel_hi:[0,0,0]
	v_mfma_scale_f32_16x16x128_f8f6f4 v[70:73], v[10:17], v[34:41], v[70:73], v211, v210 op_sel_hi:[0,0,0]
	v_mfma_scale_f32_16x16x128_f8f6f4 v[62:65], v[2:9], v[42:49], v[62:65], v211, v210 op_sel_hi:[0,0,0]
	v_mfma_scale_f32_16x16x128_f8f6f4 v[54:57], v[10:17], v[42:49], v[54:57], v211, v210 op_sel_hi:[0,0,0]
	s_setprio 0
	s_barrier
	s_add_u32 s28, s28, 0x40080
	s_addc_u32 s29, s29, 0
	s_add_i32 s34, s62, s40
	v_lshl_add_u64 v[2:3], s[28:29], 0, v[188:189]
	s_mov_b32 m0, s34
	s_nop 0
	global_load_lds_dwordx4 v[2:3], off
	v_lshl_add_u64 v[2:3], s[28:29], 0, v[186:187]
	s_add_i32 m0, s34, 0x2000
	s_nop 0
	global_load_lds_dwordx4 v[2:3], off
	s_waitcnt vmcnt(6)
	s_barrier
	s_setprio 1
	v_mfma_scale_f32_16x16x128_f8f6f4 v[106:109], v[214:221], v[18:25], v[106:109], v211, v210 op_sel_hi:[0,0,0]
	ds_read_b128 v[2:5], v206
	ds_read_b128 v[10:13], v206 offset:2048
	ds_read_b128 v[6:9], v207
	ds_read_b128 v[14:17], v207 offset:2048
	v_mfma_scale_f32_16x16x128_f8f6f4 v[98:101], v[222:229], v[18:25], v[98:101], v211, v210 op_sel_hi:[0,0,0]
	ds_read_b128 v[18:21], v208 offset:2048
	ds_read_b128 v[22:25], v209 offset:2048
	v_mfma_scale_f32_16x16x128_f8f6f4 v[90:93], v[214:221], v[26:33], v[90:93], v211, v210 op_sel_hi:[0,0,0]
	v_mfma_scale_f32_16x16x128_f8f6f4 v[82:85], v[222:229], v[26:33], v[82:85], v211, v210 op_sel_hi:[0,0,0]
	ds_read_b128 v[26:29], v208
	ds_read_b128 v[30:33], v209
	v_mfma_scale_f32_16x16x128_f8f6f4 v[74:77], v[214:221], v[34:41], v[74:77], v211, v210 op_sel_hi:[0,0,0]
	v_mfma_scale_f32_16x16x128_f8f6f4 v[66:69], v[222:229], v[34:41], v[66:69], v211, v210 op_sel_hi:[0,0,0]
	ds_read_b128 v[34:37], v208 offset:6144
	ds_read_b128 v[38:41], v209 offset:6144
	v_mfma_scale_f32_16x16x128_f8f6f4 v[58:61], v[214:221], v[42:49], v[58:61], v211, v210 op_sel_hi:[0,0,0]
	v_mfma_scale_f32_16x16x128_f8f6f4 v[50:53], v[222:229], v[42:49], v[50:53], v211, v210 op_sel_hi:[0,0,0]
	ds_read_b128 v[42:45], v208 offset:4096
	ds_read_b128 v[46:49], v209 offset:4096
	s_setprio 0
	s_cmp_ge_i32 s71, s39
	s_barrier
	s_cbranch_scc1 .LBB0_1546
	s_mov_b64 s[28:29], s[30:31]
	s_branch .LBB0_1551

.LBB0_1553:
	s_add_i32 s71, s71, 2
	s_add_u32 s30, s28, 0x100
	s_addc_u32 s31, s29, 0
	s_and_b64 s[36:37], s[34:35], exec
	s_cselect_b32 s36, 0, s30
	s_cselect_b32 s37, 0, s31
	s_add_u32 s36, s22, s36
	s_addc_u32 s37, s23, s37
	s_add_u32 s72, s69, s28
	s_addc_u32 s73, s70, s29
	s_and_b64 s[28:29], s[34:35], exec
	s_cselect_b32 s29, s67, s73
	s_cselect_b32 s28, s68, s72
	s_mov_b32 m0, s42
	v_add_u32_e32 v191, s57, v204
	v_lshl_add_u64 v[230:231], s[28:29], 0, v[188:189]
	v_add_u32_e32 v197, s57, v205
	ds_read_b128 v[214:217], v191
	ds_read_b128 v[222:225], v191 offset:2048
	ds_read_b128 v[218:221], v197
	ds_read_b128 v[226:229], v197 offset:2048
	global_load_lds_dwordx4 v[230:231], off
	v_lshl_add_u64 v[232:233], s[28:29], 0, v[186:187]
	s_mov_b32 m0, s43
	v_mfma_scale_f32_16x16x128_f8f6f4 v[174:177], v[2:9], v[26:33], v[174:177], v211, v210 op_sel_hi:[0,0,0]
	global_load_lds_dwordx4 v[232:233], off
	s_barrier
	v_mov_b32_e32 v193, v185
	v_mov_b32_e32 v195, v185
	v_mfma_scale_f32_16x16x128_f8f6f4 v[170:173], v[10:17], v[26:33], v[170:173], v211, v210 op_sel_hi:[0,0,0]
	v_mfma_scale_f32_16x16x128_f8f6f4 v[166:169], v[2:9], v[18:25], v[166:169], v211, v210 op_sel_hi:[0,0,0]
	v_mfma_scale_f32_16x16x128_f8f6f4 v[162:165], v[10:17], v[18:25], v[162:165], v211, v210 op_sel_hi:[0,0,0]
	v_mfma_scale_f32_16x16x128_f8f6f4 v[142:145], v[2:9], v[42:49], v[142:145], v211, v210 op_sel_hi:[0,0,0]
	v_mfma_scale_f32_16x16x128_f8f6f4 v[130:133], v[10:17], v[42:49], v[130:133], v211, v210 op_sel_hi:[0,0,0]
	v_mfma_scale_f32_16x16x128_f8f6f4 v[118:121], v[2:9], v[34:41], v[118:121], v211, v210 op_sel_hi:[0,0,0]
	v_mfma_scale_f32_16x16x128_f8f6f4 v[114:117], v[10:17], v[34:41], v[114:117], v211, v210 op_sel_hi:[0,0,0]
	s_setprio 1
	s_waitcnt lgkmcnt(0)
	v_mfma_scale_f32_16x16x128_f8f6f4 v[158:161], v[214:221], v[26:33], v[158:161], v211, v210 op_sel_hi:[0,0,0]
	v_mfma_scale_f32_16x16x128_f8f6f4 v[154:157], v[222:229], v[26:33], v[154:157], v211, v210 op_sel_hi:[0,0,0]
	ds_read_b128 v[26:29], v208 offset:18432
	ds_read_b128 v[30:33], v209 offset:18432
	v_mfma_scale_f32_16x16x128_f8f6f4 v[150:153], v[214:221], v[18:25], v[150:153], v211, v210 op_sel_hi:[0,0,0]
	v_mfma_scale_f32_16x16x128_f8f6f4 v[146:149], v[222:229], v[18:25], v[146:149], v211, v210 op_sel_hi:[0,0,0]
	ds_read_b128 v[18:21], v208 offset:16384
	ds_read_b128 v[22:25], v209 offset:16384
	v_mfma_scale_f32_16x16x128_f8f6f4 v[138:141], v[214:221], v[42:49], v[138:141], v211, v210 op_sel_hi:[0,0,0]
	v_mfma_scale_f32_16x16x128_f8f6f4 v[134:137], v[222:229], v[42:49], v[134:137], v211, v210 op_sel_hi:[0,0,0]
	ds_read_b128 v[42:45], v208 offset:22528
	ds_read_b128 v[46:49], v209 offset:22528
	v_mfma_scale_f32_16x16x128_f8f6f4 v[126:129], v[214:221], v[34:41], v[126:129], v211, v210 op_sel_hi:[0,0,0]
	v_mfma_scale_f32_16x16x128_f8f6f4 v[122:125], v[222:229], v[34:41], v[122:125], v211, v210 op_sel_hi:[0,0,0]
	ds_read_b128 v[34:37], v208 offset:20480
	ds_read_b128 v[38:41], v209 offset:20480
	s_setprio 0
	s_barrier
	v_mov_b32_e32 v191, v185
	s_barrier
	v_lshl_add_u64 v[234:235], s[36:37], 0, v[184:185]
	v_lshl_add_u64 v[236:237], s[36:37], 0, v[190:191]
	s_setprio 1
	s_waitcnt lgkmcnt(0)
	v_mfma_scale_f32_16x16x128_f8f6f4 v[110:113], v[2:9], v[18:25], v[110:113], v211, v210 op_sel_hi:[0,0,0]
	s_mov_b32 m0, s41
	s_nop 0
	global_load_lds_dwordx4 v184, s[36:37]
	v_mfma_scale_f32_16x16x128_f8f6f4 v[102:105], v[10:17], v[18:25], v[102:105], v211, v210 op_sel_hi:[0,0,0]
	s_mov_b32 m0, s44
	s_nop 0
	global_load_lds_dwordx4 v190, s[36:37]
	v_mfma_scale_f32_16x16x128_f8f6f4 v[94:97], v[2:9], v[26:33], v[94:97], v211, v210 op_sel_hi:[0,0,0]
	v_mfma_scale_f32_16x16x128_f8f6f4 v[86:89], v[10:17], v[26:33], v[86:89], v211, v210 op_sel_hi:[0,0,0]
	v_mfma_scale_f32_16x16x128_f8f6f4 v[78:81], v[2:9], v[34:41], v[78:81], v211, v210 op_sel_hi:[0,0,0]
	v_mfma_scale_f32_16x16x128_f8f6f4 v[70:73], v[10:17], v[34:41], v[70:73], v211, v210 op_sel_hi:[0,0,0]
	v_mfma_scale_f32_16x16x128_f8f6f4 v[62:65], v[2:9], v[42:49], v[62:65], v211, v210 op_sel_hi:[0,0,0]
	v_mfma_scale_f32_16x16x128_f8f6f4 v[54:57], v[10:17], v[42:49], v[54:57], v211, v210 op_sel_hi:[0,0,0]
	s_setprio 0
	s_barrier
	s_add_u32 s34, s28, 0x40000
	s_addc_u32 s35, s29, 0
	s_mov_b32 m0, s59
	v_lshl_add_u64 v[2:3], s[34:35], 0, v[188:189]
	global_load_lds_dwordx4 v[2:3], off
	v_lshl_add_u64 v[2:3], s[34:35], 0, v[186:187]
	s_mov_b32 m0, s60
	s_nop 0
	global_load_lds_dwordx4 v[2:3], off
	s_waitcnt vmcnt(6)
	s_barrier
	s_setprio 1
	v_mfma_scale_f32_16x16x128_f8f6f4 v[106:109], v[214:221], v[18:25], v[106:109], v211, v210 op_sel_hi:[0,0,0]
	v_mfma_scale_f32_16x16x128_f8f6f4 v[98:101], v[222:229], v[18:25], v[98:101], v211, v210 op_sel_hi:[0,0,0]
	ds_read_b128 v[18:21], v208 offset:32768
	ds_read_b128 v[22:25], v209 offset:32768
	v_mfma_scale_f32_16x16x128_f8f6f4 v[90:93], v[214:221], v[26:33], v[90:93], v211, v210 op_sel_hi:[0,0,0]
	v_mfma_scale_f32_16x16x128_f8f6f4 v[82:85], v[222:229], v[26:33], v[82:85], v211, v210 op_sel_hi:[0,0,0]
	ds_read_b128 v[26:29], v208 offset:34816
	ds_read_b128 v[30:33], v209 offset:34816
	v_mfma_scale_f32_16x16x128_f8f6f4 v[74:77], v[214:221], v[34:41], v[74:77], v211, v210 op_sel_hi:[0,0,0]
	v_mfma_scale_f32_16x16x128_f8f6f4 v[66:69], v[222:229], v[34:41], v[66:69], v211, v210 op_sel_hi:[0,0,0]
	ds_read_b128 v[34:37], v208 offset:36864
	ds_read_b128 v[38:41], v209 offset:36864
	v_mfma_scale_f32_16x16x128_f8f6f4 v[58:61], v[214:221], v[42:49], v[58:61], v211, v210 op_sel_hi:[0,0,0]
	v_mfma_scale_f32_16x16x128_f8f6f4 v[50:53], v[222:229], v[42:49], v[50:53], v211, v210 op_sel_hi:[0,0,0]
	ds_read_b128 v[42:45], v208 offset:38912
	ds_read_b128 v[46:49], v209 offset:38912
	s_setprio 0
	v_add_u32_e32 v6, s61, v204
	v_add_u32_e32 v14, s61, v205
	s_barrier
	ds_read_b128 v[2:5], v6
	ds_read_b128 v[10:13], v6 offset:2048
	ds_read_b128 v[6:9], v14
	ds_read_b128 v[14:17], v14 offset:2048
	s_waitcnt lgkmcnt(8)
	s_barrier
	s_setprio 1
	s_waitcnt lgkmcnt(0)
	v_mfma_scale_f32_16x16x128_f8f6f4 v[174:177], v[2:9], v[18:25], v[174:177], v211, v210 op_sel_hi:[0,0,0]
	s_mov_b32 m0, s45
	v_lshl_add_u64 v[214:215], s[36:37], 0, v[192:193]
	s_nop 0
	global_load_lds_dwordx4 v[214:215], off
	v_mfma_scale_f32_16x16x128_f8f6f4 v[170:173], v[10:17], v[18:25], v[170:173], v211, v210 op_sel_hi:[0,0,0]
	v_lshl_add_u64 v[214:215], s[36:37], 0, v[194:195]
	s_mov_b32 m0, s46
	s_nop 0
	global_load_lds_dwordx4 v[214:215], off
	v_mfma_scale_f32_16x16x128_f8f6f4 v[166:169], v[2:9], v[26:33], v[166:169], v211, v210 op_sel_hi:[0,0,0]
	v_mfma_scale_f32_16x16x128_f8f6f4 v[162:165], v[10:17], v[26:33], v[162:165], v211, v210 op_sel_hi:[0,0,0]
	v_mfma_scale_f32_16x16x128_f8f6f4 v[142:145], v[2:9], v[34:41], v[142:145], v211, v210 op_sel_hi:[0,0,0]
	v_mfma_scale_f32_16x16x128_f8f6f4 v[130:133], v[10:17], v[34:41], v[130:133], v211, v210 op_sel_hi:[0,0,0]
	v_mfma_scale_f32_16x16x128_f8f6f4 v[118:121], v[2:9], v[42:49], v[118:121], v211, v210 op_sel_hi:[0,0,0]
	v_mfma_scale_f32_16x16x128_f8f6f4 v[114:117], v[10:17], v[42:49], v[114:117], v211, v210 op_sel_hi:[0,0,0]
	s_setprio 0
	s_barrier
	v_add_u32_e32 v191, s62, v204
	v_add_u32_e32 v193, s62, v205
	ds_read_b128 v[214:217], v191
	ds_read_b128 v[222:225], v191 offset:2048
	ds_read_b128 v[218:221], v193
	ds_read_b128 v[226:229], v193 offset:2048
	s_barrier
	s_setprio 1
	s_waitcnt lgkmcnt(0)
	v_mfma_scale_f32_16x16x128_f8f6f4 v[158:161], v[214:221], v[18:25], v[158:161], v211, v210 op_sel_hi:[0,0,0]
	s_mov_b32 m0, s63
	v_lshl_add_u64 v[230:231], v[230:231], 0, s[12:13]
	s_nop 0
	global_load_lds_dwordx4 v[230:231], off
	v_mfma_scale_f32_16x16x128_f8f6f4 v[154:157], v[222:229], v[18:25], v[154:157], v211, v210 op_sel_hi:[0,0,0]
	v_lshl_add_u64 v[230:231], v[232:233], 0, s[12:13]
	s_add_i32 m0, s63, 0x2000
	s_nop 0
	global_load_lds_dwordx4 v[230:231], off
	ds_read_b128 v[18:21], v208 offset:49152
	ds_read_b128 v[22:25], v209 offset:49152
	v_mfma_scale_f32_16x16x128_f8f6f4 v[150:153], v[214:221], v[26:33], v[150:153], v211, v210 op_sel_hi:[0,0,0]
	v_mfma_scale_f32_16x16x128_f8f6f4 v[146:149], v[222:229], v[26:33], v[146:149], v211, v210 op_sel_hi:[0,0,0]
	ds_read_b128 v[26:29], v208 offset:51200
	ds_read_b128 v[30:33], v209 offset:51200
	v_mfma_scale_f32_16x16x128_f8f6f4 v[138:141], v[214:221], v[34:41], v[138:141], v211, v210 op_sel_hi:[0,0,0]
	v_mfma_scale_f32_16x16x128_f8f6f4 v[134:137], v[222:229], v[34:41], v[134:137], v211, v210 op_sel_hi:[0,0,0]
	ds_read_b128 v[34:37], v208 offset:53248
	ds_read_b128 v[38:41], v209 offset:53248
	v_mfma_scale_f32_16x16x128_f8f6f4 v[126:129], v[214:221], v[42:49], v[126:129], v211, v210 op_sel_hi:[0,0,0]
	v_mfma_scale_f32_16x16x128_f8f6f4 v[122:125], v[222:229], v[42:49], v[122:125], v211, v210 op_sel_hi:[0,0,0]
	ds_read_b128 v[42:45], v208 offset:55296
	ds_read_b128 v[46:49], v209 offset:55296
	s_setprio 0
	s_barrier
	s_barrier
	s_setprio 1
	s_waitcnt lgkmcnt(0)
	v_mfma_scale_f32_16x16x128_f8f6f4 v[110:113], v[2:9], v[18:25], v[110:113], v211, v210 op_sel_hi:[0,0,0]
	s_mov_b32 m0, s49
	v_lshl_add_u64 v[230:231], v[234:235], 0, s[12:13]
	s_nop 0
	global_load_lds_dwordx4 v[230:231], off
	v_mfma_scale_f32_16x16x128_f8f6f4 v[102:105], v[10:17], v[18:25], v[102:105], v211, v210 op_sel_hi:[0,0,0]
	v_lshl_add_u64 v[230:231], v[236:237], 0, s[12:13]
	s_mov_b32 m0, s50
	s_nop 0
	global_load_lds_dwordx4 v[230:231], off
	v_mfma_scale_f32_16x16x128_f8f6f4 v[94:97], v[2:9], v[26:33], v[94:97], v211, v210 op_sel_hi:[0,0,0]
	v_mfma_scale_f32_16x16x128_f8f6f4 v[86:89], v[10:17], v[26:33], v[86:89], v211, v210 op_sel_hi:[0,0,0]
	v_mfma_scale_f32_16x16x128_f8f6f4 v[78:81], v[2:9], v[34:41], v[78:81], v211, v210 op_sel_hi:[0,0,0]
	v_mfma_scale_f32_16x16x128_f8f6f4 v[70:73], v[10:17], v[34:41], v[70:73], v211, v210 op_sel_hi:[0,0,0]
	v_mfma_scale_f32_16x16x128_f8f6f4 v[62:65], v[2:9], v[42:49], v[62:65], v211, v210 op_sel_hi:[0,0,0]
	v_mfma_scale_f32_16x16x128_f8f6f4 v[54:57], v[10:17], v[42:49], v[54:57], v211, v210 op_sel_hi:[0,0,0]
	s_setprio 0
	s_barrier
	s_add_u32 s28, s28, 0x40080
	s_addc_u32 s29, s29, 0
	s_add_i32 s34, s62, s40
	v_lshl_add_u64 v[2:3], s[28:29], 0, v[188:189]
	s_mov_b32 m0, s34
	s_nop 0
	global_load_lds_dwordx4 v[2:3], off
	v_lshl_add_u64 v[2:3], s[28:29], 0, v[186:187]
	s_add_i32 m0, s34, 0x2000
	s_nop 0
	global_load_lds_dwordx4 v[2:3], off
	s_waitcnt vmcnt(6)
	s_barrier
	s_setprio 1
	v_mfma_scale_f32_16x16x128_f8f6f4 v[106:109], v[214:221], v[18:25], v[106:109], v211, v210 op_sel_hi:[0,0,0]
	ds_read_b128 v[2:5], v206
	ds_read_b128 v[10:13], v206 offset:2048
	ds_read_b128 v[6:9], v207
	ds_read_b128 v[14:17], v207 offset:2048
	v_mfma_scale_f32_16x16x128_f8f6f4 v[98:101], v[222:229], v[18:25], v[98:101], v211, v210 op_sel_hi:[0,0,0]
	ds_read_b128 v[18:21], v208 offset:2048
	ds_read_b128 v[22:25], v209 offset:2048
	v_mfma_scale_f32_16x16x128_f8f6f4 v[90:93], v[214:221], v[26:33], v[90:93], v211, v210 op_sel_hi:[0,0,0]
	v_mfma_scale_f32_16x16x128_f8f6f4 v[82:85], v[222:229], v[26:33], v[82:85], v211, v210 op_sel_hi:[0,0,0]
	ds_read_b128 v[26:29], v208
	ds_read_b128 v[30:33], v209
	v_mfma_scale_f32_16x16x128_f8f6f4 v[74:77], v[214:221], v[34:41], v[74:77], v211, v210 op_sel_hi:[0,0,0]
	v_mfma_scale_f32_16x16x128_f8f6f4 v[66:69], v[222:229], v[34:41], v[66:69], v211, v210 op_sel_hi:[0,0,0]
	ds_read_b128 v[34:37], v208 offset:6144
	ds_read_b128 v[38:41], v209 offset:6144
	v_mfma_scale_f32_16x16x128_f8f6f4 v[58:61], v[214:221], v[42:49], v[58:61], v211, v210 op_sel_hi:[0,0,0]
	v_mfma_scale_f32_16x16x128_f8f6f4 v[50:53], v[222:229], v[42:49], v[50:53], v211, v210 op_sel_hi:[0,0,0]
	ds_read_b128 v[42:45], v208 offset:4096
	ds_read_b128 v[46:49], v209 offset:4096
	s_setprio 0
	s_cmp_ge_i32 s71, s39
	s_barrier
	s_cbranch_scc1 .LBB0_1546
	s_mov_b64 s[28:29], s[30:31]
	s_branch .LBB0_1551

.Lmy_pl3_1675:
	s_add_i32 s59, s59, 2
	s_add_u32 s24, s22, 0x100
	s_addc_u32 s25, s23, 0
	s_and_b64 s[28:29], s[26:27], exec
	s_cselect_b32 s28, 0, s24
	s_cselect_b32 s29, 0, s25
	s_add_u32 s28, s12, s28
	s_addc_u32 s29, s13, s29
	s_add_u32 s60, s57, s22
	s_addc_u32 s61, s58, s23
	s_and_b64 s[22:23], s[26:27], exec
	s_cselect_b32 s23, s55, s61
	s_cselect_b32 s22, s56, s60
	s_mov_b32 m0, s5
	s_waitcnt lgkmcnt(0)
	v_mfma_scale_f32_16x16x128_f8f6f4 v[222:225], v[2:9], v[42:49], 0, v209, v208 op_sel_hi:[0,0,0]
	v_lshl_add_u64 v[238:239], s[22:23], 0, v[188:189]
	v_add_u32_e32 v191, s46, v203
	v_lshl_add_u64 v[240:241], s[22:23], 0, v[186:187]
	v_mov_b32_e32 v193, v185
	v_mov_b32_e32 v195, v185
	s_nop 1
	v_add_u32_e32 v142, s46, v202
	v_mfma_scale_f32_16x16x128_f8f6f4 v[226:229], v[10:17], v[42:49], 0, v209, v208 op_sel_hi:[0,0,0]
	s_nop 6
	ds_read_b128 v[138:141], v142
	ds_read_b128 v[214:217], v142 offset:2048
	ds_read_b128 v[142:145], v191
	ds_read_b128 v[218:221], v191 offset:2048
	global_load_lds_dwordx4 v[238:239], off
	s_mov_b32 m0, s31
	s_nop 0
	global_load_lds_dwordx4 v[240:241], off
	v_mfma_scale_f32_16x16x128_f8f6f4 v[174:177], v[2:9], v[26:33], 0, v209, v208 op_sel_hi:[0,0,0]
	s_barrier
	v_mfma_scale_f32_16x16x128_f8f6f4 v[170:173], v[10:17], v[26:33], 0, v209, v208 op_sel_hi:[0,0,0]
	v_mfma_scale_f32_16x16x128_f8f6f4 v[166:169], v[2:9], v[18:25], 0, v209, v208 op_sel_hi:[0,0,0]
	v_mfma_scale_f32_16x16x128_f8f6f4 v[162:165], v[10:17], v[18:25], 0, v209, v208 op_sel_hi:[0,0,0]
	v_mfma_scale_f32_16x16x128_f8f6f4 v[134:137], v[2:9], v[34:41], 0, v209, v208 op_sel_hi:[0,0,0]
	v_mfma_scale_f32_16x16x128_f8f6f4 v[122:125], v[10:17], v[34:41], 0, v209, v208 op_sel_hi:[0,0,0]
	s_setprio 1
	s_waitcnt lgkmcnt(0)
	v_mfma_scale_f32_16x16x128_f8f6f4 v[158:161], v[138:145], v[26:33], 0, v209, v208 op_sel_hi:[0,0,0]
	v_mfma_scale_f32_16x16x128_f8f6f4 v[154:157], v[214:221], v[26:33], 0, v209, v208 op_sel_hi:[0,0,0]
	ds_read_b128 v[26:29], v206 offset:18432
	ds_read_b128 v[30:33], v207 offset:18432
	v_mfma_scale_f32_16x16x128_f8f6f4 v[150:153], v[138:145], v[18:25], 0, v209, v208 op_sel_hi:[0,0,0]
	v_mfma_scale_f32_16x16x128_f8f6f4 v[146:149], v[214:221], v[18:25], 0, v209, v208 op_sel_hi:[0,0,0]
	ds_read_b128 v[18:21], v206 offset:16384
	ds_read_b128 v[22:25], v207 offset:16384
	v_mfma_scale_f32_16x16x128_f8f6f4 v[130:133], v[138:145], v[42:49], 0, v209, v208 op_sel_hi:[0,0,0]
	v_mfma_scale_f32_16x16x128_f8f6f4 v[126:129], v[214:221], v[42:49], 0, v209, v208 op_sel_hi:[0,0,0]
	ds_read_b128 v[42:45], v206 offset:22528
	ds_read_b128 v[46:49], v207 offset:22528
	v_mfma_scale_f32_16x16x128_f8f6f4 v[118:121], v[138:145], v[34:41], 0, v209, v208 op_sel_hi:[0,0,0]
	v_mfma_scale_f32_16x16x128_f8f6f4 v[114:117], v[214:221], v[34:41], 0, v209, v208 op_sel_hi:[0,0,0]
	ds_read_b128 v[34:37], v206 offset:20480
	ds_read_b128 v[38:41], v207 offset:20480
	s_setprio 0
	s_barrier
	v_mov_b32_e32 v191, v185
	s_barrier
	v_lshl_add_u64 v[242:243], s[28:29], 0, v[184:185]
	v_lshl_add_u64 v[244:245], s[28:29], 0, v[190:191]
	s_setprio 1
	s_waitcnt lgkmcnt(0)
	v_mfma_scale_f32_16x16x128_f8f6f4 v[110:113], v[2:9], v[18:25], 0, v209, v208 op_sel_hi:[0,0,0]
	s_mov_b32 m0, s4
	s_nop 0
	global_load_lds_dwordx4 v184, s[28:29]
	v_mfma_scale_f32_16x16x128_f8f6f4 v[106:109], v[10:17], v[18:25], 0, v209, v208 op_sel_hi:[0,0,0]
	s_mov_b32 m0, s33
	s_nop 0
	global_load_lds_dwordx4 v190, s[28:29]
	v_mfma_scale_f32_16x16x128_f8f6f4 v[102:105], v[2:9], v[26:33], 0, v209, v208 op_sel_hi:[0,0,0]
	v_mfma_scale_f32_16x16x128_f8f6f4 v[98:101], v[10:17], v[26:33], 0, v209, v208 op_sel_hi:[0,0,0]
	v_mfma_scale_f32_16x16x128_f8f6f4 v[78:81], v[2:9], v[34:41], 0, v209, v208 op_sel_hi:[0,0,0]
	v_mfma_scale_f32_16x16x128_f8f6f4 v[74:77], v[10:17], v[34:41], 0, v209, v208 op_sel_hi:[0,0,0]
	v_mfma_scale_f32_16x16x128_f8f6f4 v[70:73], v[2:9], v[42:49], 0, v209, v208 op_sel_hi:[0,0,0]
	v_mfma_scale_f32_16x16x128_f8f6f4 v[66:69], v[10:17], v[42:49], 0, v209, v208 op_sel_hi:[0,0,0]
	s_setprio 0
	s_barrier
	s_add_u32 s26, s22, 0x10000
	s_addc_u32 s27, s23, 0
	s_mov_b32 m0, s48
	v_lshl_add_u64 v[2:3], s[26:27], 0, v[188:189]
	global_load_lds_dwordx4 v[2:3], off
	v_lshl_add_u64 v[2:3], s[26:27], 0, v[186:187]
	s_mov_b32 m0, s49
	s_nop 0
	global_load_lds_dwordx4 v[2:3], off
	s_waitcnt vmcnt(6)
	s_barrier
	s_setprio 1
	v_mfma_scale_f32_16x16x128_f8f6f4 v[94:97], v[138:145], v[18:25], 0, v209, v208 op_sel_hi:[0,0,0]
	v_mfma_scale_f32_16x16x128_f8f6f4 v[90:93], v[214:221], v[18:25], 0, v209, v208 op_sel_hi:[0,0,0]
	ds_read_b128 v[18:21], v206 offset:32768
	ds_read_b128 v[22:25], v207 offset:32768
	v_mfma_scale_f32_16x16x128_f8f6f4 v[86:89], v[138:145], v[26:33], 0, v209, v208 op_sel_hi:[0,0,0]
	v_mfma_scale_f32_16x16x128_f8f6f4 v[82:85], v[214:221], v[26:33], 0, v209, v208 op_sel_hi:[0,0,0]
	ds_read_b128 v[26:29], v206 offset:34816
	ds_read_b128 v[30:33], v207 offset:34816
	v_mfma_scale_f32_16x16x128_f8f6f4 v[62:65], v[138:145], v[34:41], 0, v209, v208 op_sel_hi:[0,0,0]
	v_mfma_scale_f32_16x16x128_f8f6f4 v[58:61], v[214:221], v[34:41], 0, v209, v208 op_sel_hi:[0,0,0]
	ds_read_b128 v[34:37], v206 offset:36864
	ds_read_b128 v[38:41], v207 offset:36864
	v_mfma_scale_f32_16x16x128_f8f6f4 v[230:233], v[138:145], v[42:49], 0, v209, v208 op_sel_hi:[0,0,0]
	v_mfma_scale_f32_16x16x128_f8f6f4 v[234:237], v[214:221], v[42:49], 0, v209, v208 op_sel_hi:[0,0,0]
	ds_read_b128 v[42:45], v206 offset:38912
	ds_read_b128 v[46:49], v207 offset:38912
	s_setprio 0
	v_add_u32_e32 v6, s50, v202
	v_add_u32_e32 v14, s50, v203
	s_barrier
	ds_read_b128 v[2:5], v6
	ds_read_b128 v[10:13], v6 offset:2048
	ds_read_b128 v[6:9], v14
	ds_read_b128 v[14:17], v14 offset:2048
	s_waitcnt lgkmcnt(8)
	s_barrier
	s_setprio 1
	s_waitcnt lgkmcnt(0)
	v_mfma_scale_f32_16x16x128_f8f6f4 v[174:177], v[2:9], v[18:25], v[174:177], v209, v208 op_sel_hi:[0,0,0]
	s_mov_b32 m0, s34
	v_lshl_add_u64 v[50:51], s[28:29], 0, v[192:193]
	s_nop 0
	global_load_lds_dwordx4 v[50:51], off
	v_mfma_scale_f32_16x16x128_f8f6f4 v[170:173], v[10:17], v[18:25], v[170:173], v209, v208 op_sel_hi:[0,0,0]
	v_lshl_add_u64 v[50:51], s[28:29], 0, v[194:195]
	s_mov_b32 m0, s35
	s_nop 0
	global_load_lds_dwordx4 v[50:51], off
	v_mfma_scale_f32_16x16x128_f8f6f4 v[166:169], v[2:9], v[26:33], v[166:169], v209, v208 op_sel_hi:[0,0,0]
	v_mfma_scale_f32_16x16x128_f8f6f4 v[162:165], v[10:17], v[26:33], v[162:165], v209, v208 op_sel_hi:[0,0,0]
	v_mfma_scale_f32_16x16x128_f8f6f4 v[142:145], v[2:9], v[34:41], v[222:225], v209, v208 op_sel_hi:[0,0,0]
	v_mfma_scale_f32_16x16x128_f8f6f4 v[138:141], v[10:17], v[34:41], v[226:229], v209, v208 op_sel_hi:[0,0,0]
	v_mfma_scale_f32_16x16x128_f8f6f4 v[134:137], v[2:9], v[42:49], v[134:137], v209, v208 op_sel_hi:[0,0,0]
	v_mfma_scale_f32_16x16x128_f8f6f4 v[122:125], v[10:17], v[42:49], v[122:125], v209, v208 op_sel_hi:[0,0,0]
	s_setprio 0
	s_barrier
	v_add_u32_e32 v54, s51, v202
	v_add_u32_e32 v191, s51, v203
	ds_read_b128 v[50:53], v54
	ds_read_b128 v[214:217], v54 offset:2048
	ds_read_b128 v[54:57], v191
	ds_read_b128 v[218:221], v191 offset:2048
	s_barrier
	s_setprio 1
	s_waitcnt lgkmcnt(0)
	v_mfma_scale_f32_16x16x128_f8f6f4 v[158:161], v[50:57], v[18:25], v[158:161], v209, v208 op_sel_hi:[0,0,0]
	s_mov_b32 m0, s52
	v_lshl_add_u64 v[222:223], v[238:239], 0, s[8:9]
	s_nop 0
	global_load_lds_dwordx4 v[222:223], off
	v_mfma_scale_f32_16x16x128_f8f6f4 v[154:157], v[214:221], v[18:25], v[154:157], v209, v208 op_sel_hi:[0,0,0]
	v_lshl_add_u64 v[222:223], v[240:241], 0, s[8:9]
	s_mov_b32 m0, s53
	s_nop 0
	global_load_lds_dwordx4 v[222:223], off
	ds_read_b128 v[18:21], v206 offset:49152
	ds_read_b128 v[22:25], v207 offset:49152
	v_mfma_scale_f32_16x16x128_f8f6f4 v[150:153], v[50:57], v[26:33], v[150:153], v209, v208 op_sel_hi:[0,0,0]
	v_mfma_scale_f32_16x16x128_f8f6f4 v[146:149], v[214:221], v[26:33], v[146:149], v209, v208 op_sel_hi:[0,0,0]
	ds_read_b128 v[26:29], v206 offset:51200
	ds_read_b128 v[30:33], v207 offset:51200
	v_mfma_scale_f32_16x16x128_f8f6f4 v[130:133], v[50:57], v[34:41], v[130:133], v209, v208 op_sel_hi:[0,0,0]
	v_mfma_scale_f32_16x16x128_f8f6f4 v[126:129], v[214:221], v[34:41], v[126:129], v209, v208 op_sel_hi:[0,0,0]
	ds_read_b128 v[34:37], v206 offset:53248
	ds_read_b128 v[38:41], v207 offset:53248
	v_mfma_scale_f32_16x16x128_f8f6f4 v[118:121], v[50:57], v[42:49], v[118:121], v209, v208 op_sel_hi:[0,0,0]
	v_mfma_scale_f32_16x16x128_f8f6f4 v[114:117], v[214:221], v[42:49], v[114:117], v209, v208 op_sel_hi:[0,0,0]
	ds_read_b128 v[42:45], v206 offset:55296
	ds_read_b128 v[46:49], v207 offset:55296
	s_setprio 0
	s_barrier
	s_barrier
	s_setprio 1
	s_waitcnt lgkmcnt(0)
	v_mfma_scale_f32_16x16x128_f8f6f4 v[110:113], v[2:9], v[18:25], v[110:113], v209, v208 op_sel_hi:[0,0,0]
	s_mov_b32 m0, s38
	v_lshl_add_u64 v[222:223], v[242:243], 0, s[8:9]
	s_nop 0
	global_load_lds_dwordx4 v[222:223], off
	v_mfma_scale_f32_16x16x128_f8f6f4 v[106:109], v[10:17], v[18:25], v[106:109], v209, v208 op_sel_hi:[0,0,0]
	v_lshl_add_u64 v[222:223], v[244:245], 0, s[8:9]
	s_mov_b32 m0, s39
	s_nop 0
	global_load_lds_dwordx4 v[222:223], off
	v_mfma_scale_f32_16x16x128_f8f6f4 v[102:105], v[2:9], v[26:33], v[102:105], v209, v208 op_sel_hi:[0,0,0]
	v_mfma_scale_f32_16x16x128_f8f6f4 v[98:101], v[10:17], v[26:33], v[98:101], v209, v208 op_sel_hi:[0,0,0]
	v_mfma_scale_f32_16x16x128_f8f6f4 v[78:81], v[2:9], v[34:41], v[78:81], v209, v208 op_sel_hi:[0,0,0]
	v_mfma_scale_f32_16x16x128_f8f6f4 v[74:77], v[10:17], v[34:41], v[74:77], v209, v208 op_sel_hi:[0,0,0]
	v_mfma_scale_f32_16x16x128_f8f6f4 v[70:73], v[2:9], v[42:49], v[70:73], v209, v208 op_sel_hi:[0,0,0]
	v_mfma_scale_f32_16x16x128_f8f6f4 v[66:69], v[10:17], v[42:49], v[66:69], v209, v208 op_sel_hi:[0,0,0]
	s_setprio 0
	s_barrier
	s_add_u32 s22, s22, 0x10080
	s_addc_u32 s23, s23, 0
	s_mov_b32 m0, s54
	v_lshl_add_u64 v[2:3], s[22:23], 0, v[188:189]
	global_load_lds_dwordx4 v[2:3], off
	v_lshl_add_u64 v[2:3], s[22:23], 0, v[186:187]
	s_add_i32 m0, s54, 0x2000
	s_nop 0
	global_load_lds_dwordx4 v[2:3], off
	s_waitcnt vmcnt(6)
	s_barrier
	s_setprio 1
	v_mfma_scale_f32_16x16x128_f8f6f4 v[94:97], v[50:57], v[18:25], v[94:97], v209, v208 op_sel_hi:[0,0,0]
	ds_read_b128 v[2:5], v204
	ds_read_b128 v[10:13], v204 offset:2048
	ds_read_b128 v[6:9], v205
	ds_read_b128 v[14:17], v205 offset:2048
	v_mfma_scale_f32_16x16x128_f8f6f4 v[90:93], v[214:221], v[18:25], v[90:93], v209, v208 op_sel_hi:[0,0,0]
	ds_read_b128 v[18:21], v206 offset:2048
	ds_read_b128 v[22:25], v207 offset:2048
	v_mfma_scale_f32_16x16x128_f8f6f4 v[86:89], v[50:57], v[26:33], v[86:89], v209, v208 op_sel_hi:[0,0,0]
	v_mfma_scale_f32_16x16x128_f8f6f4 v[82:85], v[214:221], v[26:33], v[82:85], v209, v208 op_sel_hi:[0,0,0]
	ds_read_b128 v[26:29], v206
	ds_read_b128 v[30:33], v207
	v_mfma_scale_f32_16x16x128_f8f6f4 v[62:65], v[50:57], v[34:41], v[62:65], v209, v208 op_sel_hi:[0,0,0]
	v_mfma_scale_f32_16x16x128_f8f6f4 v[58:61], v[214:221], v[34:41], v[58:61], v209, v208 op_sel_hi:[0,0,0]
	ds_read_b128 v[34:37], v206 offset:6144
	ds_read_b128 v[38:41], v207 offset:6144
	v_mfma_scale_f32_16x16x128_f8f6f4 v[54:57], v[50:57], v[42:49], v[230:233], v209, v208 op_sel_hi:[0,0,0]
	v_mfma_scale_f32_16x16x128_f8f6f4 v[50:53], v[214:221], v[42:49], v[234:237], v209, v208 op_sel_hi:[0,0,0]
	ds_read_b128 v[42:45], v206 offset:4096
	ds_read_b128 v[46:49], v207 offset:4096
	s_setprio 0
	s_cmp_ge_i32 s59, s1
	s_barrier
	s_cbranch_scc1 .LBB0_1668
	s_mov_b64 s[22:23], s[24:25]
	s_branch .LBB0_1673

.LBB0_1675:
	s_add_i32 s59, s59, 2
	s_add_u32 s24, s22, 0x100
	s_addc_u32 s25, s23, 0
	s_and_b64 s[28:29], s[26:27], exec
	s_cselect_b32 s28, 0, s24
	s_cselect_b32 s29, 0, s25
	s_add_u32 s28, s12, s28
	s_addc_u32 s29, s13, s29
	s_add_u32 s60, s57, s22
	s_addc_u32 s61, s58, s23
	s_and_b64 s[22:23], s[26:27], exec
	s_cselect_b32 s23, s55, s61
	s_cselect_b32 s22, s56, s60
	s_mov_b32 m0, s5
	s_waitcnt lgkmcnt(0)
	v_mfma_scale_f32_16x16x128_f8f6f4 v[222:225], v[2:9], v[42:49], v[142:145], v209, v208 op_sel_hi:[0,0,0]
	v_lshl_add_u64 v[238:239], s[22:23], 0, v[188:189]
	v_add_u32_e32 v191, s46, v203
	v_lshl_add_u64 v[240:241], s[22:23], 0, v[186:187]
	v_mov_b32_e32 v193, v185
	v_mov_b32_e32 v195, v185
	s_nop 1
	v_add_u32_e32 v142, s46, v202
	v_mfma_scale_f32_16x16x128_f8f6f4 v[226:229], v[10:17], v[42:49], v[138:141], v209, v208 op_sel_hi:[0,0,0]
	s_nop 6
	ds_read_b128 v[138:141], v142
	ds_read_b128 v[214:217], v142 offset:2048
	ds_read_b128 v[142:145], v191
	ds_read_b128 v[218:221], v191 offset:2048
	global_load_lds_dwordx4 v[238:239], off
	s_mov_b32 m0, s31
	s_nop 0
	global_load_lds_dwordx4 v[240:241], off
	v_mfma_scale_f32_16x16x128_f8f6f4 v[174:177], v[2:9], v[26:33], v[174:177], v209, v208 op_sel_hi:[0,0,0]
	s_barrier
	v_mfma_scale_f32_16x16x128_f8f6f4 v[170:173], v[10:17], v[26:33], v[170:173], v209, v208 op_sel_hi:[0,0,0]
	v_mfma_scale_f32_16x16x128_f8f6f4 v[166:169], v[2:9], v[18:25], v[166:169], v209, v208 op_sel_hi:[0,0,0]
	v_mfma_scale_f32_16x16x128_f8f6f4 v[162:165], v[10:17], v[18:25], v[162:165], v209, v208 op_sel_hi:[0,0,0]
	v_mfma_scale_f32_16x16x128_f8f6f4 v[134:137], v[2:9], v[34:41], v[134:137], v209, v208 op_sel_hi:[0,0,0]
	v_mfma_scale_f32_16x16x128_f8f6f4 v[122:125], v[10:17], v[34:41], v[122:125], v209, v208 op_sel_hi:[0,0,0]
	s_setprio 1
	s_waitcnt lgkmcnt(0)
	v_mfma_scale_f32_16x16x128_f8f6f4 v[158:161], v[138:145], v[26:33], v[158:161], v209, v208 op_sel_hi:[0,0,0]
	v_mfma_scale_f32_16x16x128_f8f6f4 v[154:157], v[214:221], v[26:33], v[154:157], v209, v208 op_sel_hi:[0,0,0]
	ds_read_b128 v[26:29], v206 offset:18432
	ds_read_b128 v[30:33], v207 offset:18432
	v_mfma_scale_f32_16x16x128_f8f6f4 v[150:153], v[138:145], v[18:25], v[150:153], v209, v208 op_sel_hi:[0,0,0]
	v_mfma_scale_f32_16x16x128_f8f6f4 v[146:149], v[214:221], v[18:25], v[146:149], v209, v208 op_sel_hi:[0,0,0]
	ds_read_b128 v[18:21], v206 offset:16384
	ds_read_b128 v[22:25], v207 offset:16384
	v_mfma_scale_f32_16x16x128_f8f6f4 v[130:133], v[138:145], v[42:49], v[130:133], v209, v208 op_sel_hi:[0,0,0]
	v_mfma_scale_f32_16x16x128_f8f6f4 v[126:129], v[214:221], v[42:49], v[126:129], v209, v208 op_sel_hi:[0,0,0]
	ds_read_b128 v[42:45], v206 offset:22528
	ds_read_b128 v[46:49], v207 offset:22528
	v_mfma_scale_f32_16x16x128_f8f6f4 v[118:121], v[138:145], v[34:41], v[118:121], v209, v208 op_sel_hi:[0,0,0]
	v_mfma_scale_f32_16x16x128_f8f6f4 v[114:117], v[214:221], v[34:41], v[114:117], v209, v208 op_sel_hi:[0,0,0]
	ds_read_b128 v[34:37], v206 offset:20480
	ds_read_b128 v[38:41], v207 offset:20480
	s_setprio 0
	s_barrier
	v_mov_b32_e32 v191, v185
	s_barrier
	v_lshl_add_u64 v[242:243], s[28:29], 0, v[184:185]
	v_lshl_add_u64 v[244:245], s[28:29], 0, v[190:191]
	s_setprio 1
	s_waitcnt lgkmcnt(0)
	v_mfma_scale_f32_16x16x128_f8f6f4 v[110:113], v[2:9], v[18:25], v[110:113], v209, v208 op_sel_hi:[0,0,0]
	s_mov_b32 m0, s4
	s_nop 0
	global_load_lds_dwordx4 v184, s[28:29]
	v_mfma_scale_f32_16x16x128_f8f6f4 v[106:109], v[10:17], v[18:25], v[106:109], v209, v208 op_sel_hi:[0,0,0]
	s_mov_b32 m0, s33
	s_nop 0
	global_load_lds_dwordx4 v190, s[28:29]
	v_mfma_scale_f32_16x16x128_f8f6f4 v[102:105], v[2:9], v[26:33], v[102:105], v209, v208 op_sel_hi:[0,0,0]
	v_mfma_scale_f32_16x16x128_f8f6f4 v[98:101], v[10:17], v[26:33], v[98:101], v209, v208 op_sel_hi:[0,0,0]
	v_mfma_scale_f32_16x16x128_f8f6f4 v[78:81], v[2:9], v[34:41], v[78:81], v209, v208 op_sel_hi:[0,0,0]
	v_mfma_scale_f32_16x16x128_f8f6f4 v[74:77], v[10:17], v[34:41], v[74:77], v209, v208 op_sel_hi:[0,0,0]
	v_mfma_scale_f32_16x16x128_f8f6f4 v[70:73], v[2:9], v[42:49], v[70:73], v209, v208 op_sel_hi:[0,0,0]
	v_mfma_scale_f32_16x16x128_f8f6f4 v[66:69], v[10:17], v[42:49], v[66:69], v209, v208 op_sel_hi:[0,0,0]
	s_setprio 0
	s_barrier
	s_add_u32 s26, s22, 0x10000
	s_addc_u32 s27, s23, 0
	s_mov_b32 m0, s48
	v_lshl_add_u64 v[2:3], s[26:27], 0, v[188:189]
	global_load_lds_dwordx4 v[2:3], off
	v_lshl_add_u64 v[2:3], s[26:27], 0, v[186:187]
	s_mov_b32 m0, s49
	s_nop 0
	global_load_lds_dwordx4 v[2:3], off
	s_waitcnt vmcnt(6)
	s_barrier
	s_setprio 1
	v_mfma_scale_f32_16x16x128_f8f6f4 v[94:97], v[138:145], v[18:25], v[94:97], v209, v208 op_sel_hi:[0,0,0]
	v_mfma_scale_f32_16x16x128_f8f6f4 v[90:93], v[214:221], v[18:25], v[90:93], v209, v208 op_sel_hi:[0,0,0]
	ds_read_b128 v[18:21], v206 offset:32768
	ds_read_b128 v[22:25], v207 offset:32768
	v_mfma_scale_f32_16x16x128_f8f6f4 v[86:89], v[138:145], v[26:33], v[86:89], v209, v208 op_sel_hi:[0,0,0]
	v_mfma_scale_f32_16x16x128_f8f6f4 v[82:85], v[214:221], v[26:33], v[82:85], v209, v208 op_sel_hi:[0,0,0]
	ds_read_b128 v[26:29], v206 offset:34816
	ds_read_b128 v[30:33], v207 offset:34816
	v_mfma_scale_f32_16x16x128_f8f6f4 v[62:65], v[138:145], v[34:41], v[62:65], v209, v208 op_sel_hi:[0,0,0]
	v_mfma_scale_f32_16x16x128_f8f6f4 v[58:61], v[214:221], v[34:41], v[58:61], v209, v208 op_sel_hi:[0,0,0]
	ds_read_b128 v[34:37], v206 offset:36864
	ds_read_b128 v[38:41], v207 offset:36864
	v_mfma_scale_f32_16x16x128_f8f6f4 v[230:233], v[138:145], v[42:49], v[54:57], v209, v208 op_sel_hi:[0,0,0]
	v_mfma_scale_f32_16x16x128_f8f6f4 v[234:237], v[214:221], v[42:49], v[50:53], v209, v208 op_sel_hi:[0,0,0]
	ds_read_b128 v[42:45], v206 offset:38912
	ds_read_b128 v[46:49], v207 offset:38912
	s_setprio 0
	v_add_u32_e32 v6, s50, v202
	v_add_u32_e32 v14, s50, v203
	s_barrier
	ds_read_b128 v[2:5], v6
	ds_read_b128 v[10:13], v6 offset:2048
	ds_read_b128 v[6:9], v14
	ds_read_b128 v[14:17], v14 offset:2048
	s_waitcnt lgkmcnt(8)
	s_barrier
	s_setprio 1
	s_waitcnt lgkmcnt(0)
	v_mfma_scale_f32_16x16x128_f8f6f4 v[174:177], v[2:9], v[18:25], v[174:177], v209, v208 op_sel_hi:[0,0,0]
	s_mov_b32 m0, s34
	v_lshl_add_u64 v[50:51], s[28:29], 0, v[192:193]
	s_nop 0
	global_load_lds_dwordx4 v[50:51], off
	v_mfma_scale_f32_16x16x128_f8f6f4 v[170:173], v[10:17], v[18:25], v[170:173], v209, v208 op_sel_hi:[0,0,0]
	v_lshl_add_u64 v[50:51], s[28:29], 0, v[194:195]
	s_mov_b32 m0, s35
	s_nop 0
	global_load_lds_dwordx4 v[50:51], off
	v_mfma_scale_f32_16x16x128_f8f6f4 v[166:169], v[2:9], v[26:33], v[166:169], v209, v208 op_sel_hi:[0,0,0]
	v_mfma_scale_f32_16x16x128_f8f6f4 v[162:165], v[10:17], v[26:33], v[162:165], v209, v208 op_sel_hi:[0,0,0]
	v_mfma_scale_f32_16x16x128_f8f6f4 v[142:145], v[2:9], v[34:41], v[222:225], v209, v208 op_sel_hi:[0,0,0]
	v_mfma_scale_f32_16x16x128_f8f6f4 v[138:141], v[10:17], v[34:41], v[226:229], v209, v208 op_sel_hi:[0,0,0]
	v_mfma_scale_f32_16x16x128_f8f6f4 v[134:137], v[2:9], v[42:49], v[134:137], v209, v208 op_sel_hi:[0,0,0]
	v_mfma_scale_f32_16x16x128_f8f6f4 v[122:125], v[10:17], v[42:49], v[122:125], v209, v208 op_sel_hi:[0,0,0]
	s_setprio 0
	s_barrier
	v_add_u32_e32 v54, s51, v202
	v_add_u32_e32 v191, s51, v203
	ds_read_b128 v[50:53], v54
	ds_read_b128 v[214:217], v54 offset:2048
	ds_read_b128 v[54:57], v191
	ds_read_b128 v[218:221], v191 offset:2048
	s_barrier
	s_setprio 1
	s_waitcnt lgkmcnt(0)
	v_mfma_scale_f32_16x16x128_f8f6f4 v[158:161], v[50:57], v[18:25], v[158:161], v209, v208 op_sel_hi:[0,0,0]
	s_mov_b32 m0, s52
	v_lshl_add_u64 v[222:223], v[238:239], 0, s[8:9]
	s_nop 0
	global_load_lds_dwordx4 v[222:223], off
	v_mfma_scale_f32_16x16x128_f8f6f4 v[154:157], v[214:221], v[18:25], v[154:157], v209, v208 op_sel_hi:[0,0,0]
	v_lshl_add_u64 v[222:223], v[240:241], 0, s[8:9]
	s_mov_b32 m0, s53
	s_nop 0
	global_load_lds_dwordx4 v[222:223], off
	ds_read_b128 v[18:21], v206 offset:49152
	ds_read_b128 v[22:25], v207 offset:49152
	v_mfma_scale_f32_16x16x128_f8f6f4 v[150:153], v[50:57], v[26:33], v[150:153], v209, v208 op_sel_hi:[0,0,0]
	v_mfma_scale_f32_16x16x128_f8f6f4 v[146:149], v[214:221], v[26:33], v[146:149], v209, v208 op_sel_hi:[0,0,0]
	ds_read_b128 v[26:29], v206 offset:51200
	ds_read_b128 v[30:33], v207 offset:51200
	v_mfma_scale_f32_16x16x128_f8f6f4 v[130:133], v[50:57], v[34:41], v[130:133], v209, v208 op_sel_hi:[0,0,0]
	v_mfma_scale_f32_16x16x128_f8f6f4 v[126:129], v[214:221], v[34:41], v[126:129], v209, v208 op_sel_hi:[0,0,0]
	ds_read_b128 v[34:37], v206 offset:53248
	ds_read_b128 v[38:41], v207 offset:53248
	v_mfma_scale_f32_16x16x128_f8f6f4 v[118:121], v[50:57], v[42:49], v[118:121], v209, v208 op_sel_hi:[0,0,0]
	v_mfma_scale_f32_16x16x128_f8f6f4 v[114:117], v[214:221], v[42:49], v[114:117], v209, v208 op_sel_hi:[0,0,0]
	ds_read_b128 v[42:45], v206 offset:55296
	ds_read_b128 v[46:49], v207 offset:55296
	s_setprio 0
	s_barrier
	s_barrier
	s_setprio 1
	s_waitcnt lgkmcnt(0)
	v_mfma_scale_f32_16x16x128_f8f6f4 v[110:113], v[2:9], v[18:25], v[110:113], v209, v208 op_sel_hi:[0,0,0]
	s_mov_b32 m0, s38
	v_lshl_add_u64 v[222:223], v[242:243], 0, s[8:9]
	s_nop 0
	global_load_lds_dwordx4 v[222:223], off
	v_mfma_scale_f32_16x16x128_f8f6f4 v[106:109], v[10:17], v[18:25], v[106:109], v209, v208 op_sel_hi:[0,0,0]
	v_lshl_add_u64 v[222:223], v[244:245], 0, s[8:9]
	s_mov_b32 m0, s39
	s_nop 0
	global_load_lds_dwordx4 v[222:223], off
	v_mfma_scale_f32_16x16x128_f8f6f4 v[102:105], v[2:9], v[26:33], v[102:105], v209, v208 op_sel_hi:[0,0,0]
	v_mfma_scale_f32_16x16x128_f8f6f4 v[98:101], v[10:17], v[26:33], v[98:101], v209, v208 op_sel_hi:[0,0,0]
	v_mfma_scale_f32_16x16x128_f8f6f4 v[78:81], v[2:9], v[34:41], v[78:81], v209, v208 op_sel_hi:[0,0,0]
	v_mfma_scale_f32_16x16x128_f8f6f4 v[74:77], v[10:17], v[34:41], v[74:77], v209, v208 op_sel_hi:[0,0,0]
	v_mfma_scale_f32_16x16x128_f8f6f4 v[70:73], v[2:9], v[42:49], v[70:73], v209, v208 op_sel_hi:[0,0,0]
	v_mfma_scale_f32_16x16x128_f8f6f4 v[66:69], v[10:17], v[42:49], v[66:69], v209, v208 op_sel_hi:[0,0,0]
	s_setprio 0
	s_barrier
	s_add_u32 s22, s22, 0x10080
	s_addc_u32 s23, s23, 0
	s_mov_b32 m0, s54
	v_lshl_add_u64 v[2:3], s[22:23], 0, v[188:189]
	global_load_lds_dwordx4 v[2:3], off
	v_lshl_add_u64 v[2:3], s[22:23], 0, v[186:187]
	s_add_i32 m0, s54, 0x2000
	s_nop 0
	global_load_lds_dwordx4 v[2:3], off
	s_waitcnt vmcnt(6)
	s_barrier
	s_setprio 1
	v_mfma_scale_f32_16x16x128_f8f6f4 v[94:97], v[50:57], v[18:25], v[94:97], v209, v208 op_sel_hi:[0,0,0]
	v_mfma_scale_f32_16x16x128_f8f6f4 v[90:93], v[214:221], v[18:25], v[90:93], v209, v208 op_sel_hi:[0,0,0]
	v_mfma_scale_f32_16x16x128_f8f6f4 v[86:89], v[50:57], v[26:33], v[86:89], v209, v208 op_sel_hi:[0,0,0]
	v_mfma_scale_f32_16x16x128_f8f6f4 v[82:85], v[214:221], v[26:33], v[82:85], v209, v208 op_sel_hi:[0,0,0]
	v_mfma_scale_f32_16x16x128_f8f6f4 v[62:65], v[50:57], v[34:41], v[62:65], v209, v208 op_sel_hi:[0,0,0]
	v_mfma_scale_f32_16x16x128_f8f6f4 v[58:61], v[214:221], v[34:41], v[58:61], v209, v208 op_sel_hi:[0,0,0]
	v_mfma_scale_f32_16x16x128_f8f6f4 v[54:57], v[50:57], v[42:49], v[230:233], v209, v208 op_sel_hi:[0,0,0]
	v_mfma_scale_f32_16x16x128_f8f6f4 v[50:53], v[214:221], v[42:49], v[234:237], v209, v208 op_sel_hi:[0,0,0]
	s_setprio 0
	s_cmp_ge_i32 s59, s1
	s_barrier
	s_cbranch_scc1 .LBB0_1668
	s_mov_b64 s[22:23], s[24:25]
	s_branch .LBB0_1673
